# V-tile LDS-DMA pieces also on a scalar base advanced by SALU (two 32-bit lane offsets)
# baseline (speedup 1.0000x reference)
; DEVI int tidx() { int t = threadIdx.x; asm volatile("" : "+v"(t)); __builtin_assume(t >= 0 && t < 512); return t; }
; DEVI unsigned cvt_pk_bf16(float lo, float hi) { unsigned r; asm volatile("v_cvt_pk_bf16_f32 %0, %1, %2" : "=v"(r) : "v"(lo), "v"(hi)); return r; }
; DEVI float bf2f(bf16_t h) { return __uint_as_float(((unsigned)h) << 16); }
; DEVI void attn_unit8(const Params& p, char* smem, int unit, int l, int& cvs  , CvRun& crun) {
;     const int tid = tidx(), wid = __builtin_amdgcn_readfirstlane(tid >> 6), lane = tid & 63, r32 = lane & 31, hi = lane >> 5;
;     const int x8 = unit & 7, v8 = unit >> 3, bh = x8 + 8 * (v8 >> 4), qt = v8 & 15, b = bh >> 3, hh = bh & 7;
;     char* K_lds = smem; char* V_lds = smem + 73728;
;     float* wsx = (float*)(smem + 122880) + wid * 64; float* li_l = wsx; float* al_l = wsx + 32;
;     const bf16_t* Kg = p.kfull + (size_t)bh * S_ * 96; const bf16_t* Vg = p.vfull + (size_t)bh * S_ * 64;
;     const size_t qtok = (size_t)b * S_ + qt * 256 + wid * 32 + r32;
;     bf16x8 qr[6];
;     { const bf16_t* qp = p.qbuf + qtok * 768 + hh * 96 + hi * 8;
; #pragma unroll
;       for (int d0 = 0; d0 < 6; ++d0) qr[d0] = *(const bf16x8*)(qp + d0 * 16);
;       const f32x4 c0 = *(const f32x4*)(p.cs + qtok * 16 + hi * 8), c1 = *(const f32x4*)(p.cs + qtok * 16 + hi * 8 + 4);
;       const f32x4 s0 = *(const f32x4*)(p.sn + qtok * 16 + hi * 8), s1 = *(const f32x4*)(p.sn + qtok * 16 + hi * 8 + 4);
;       float o1[8], o2[8];
; #pragma unroll
;       for (int j = 0; j < 8; ++j) { const float x1 = bf2f((bf16_t)qr[4][j]), x2 = bf2f((bf16_t)qr[5][j]); const float cc = j < 4 ? c0[j] : c1[j - 4], ss = j < 4 ? s0[j] : s1[j - 4];
;           o1[j] = x1 * cc - x2 * ss; o2[j] = x2 * cc + x1 * ss; }
;       u32x4 w1, w2;
; #pragma unroll
;       for (int j = 0; j < 4; ++j) { w1[j] = cvt_pk_bf16(o1[2 * j], o1[2 * j + 1]); w2[j] = cvt_pk_bf16(o2[2 * j], o2[2 * j + 1]); }
;       qr[4] = *(bf16x8*)&w1; qr[5] = *(bf16x8*)&w2; }
.LBB0_665:
	v_mov_b32_e32 v86, v0
	s_ashr_i32 s5, s83, 4
	v_readfirstlane_b32 s4, v86
	s_lshr_b32 s53, s4, 6
	s_and_b32 s52, s5, -8
	s_and_b32 s8, s4, 0x3fffffc0
	s_load_dwordx4 s[4:7], s[24:25], 0x1a0
	s_load_dwordx4 s[12:15], s[24:25], 0x110
	s_and_b32 s87, s83, 7
	s_ashr_i32 s16, s83, 7
	s_lshl_b32 s8, s8, 2
	s_or_b32 s10, s52, s87
	s_add_i32 s91, s8, 0
	s_ashr_i32 s17, s16, 31
	s_lshl_b32 s8, s83, 5
	s_ashr_i32 s11, s10, 31
	s_lshl_b64 s[16:17], s[16:17], 12
	s_and_b32 s8, s8, 0xf00
	s_and_b32 s2, s62, 7
	s_add_i32 s91, s91, 0x1e000
	s_waitcnt lgkmcnt(0)
	v_mov_b32_e32 v2, s4
	v_mov_b32_e32 v3, s5
	s_lshl_b64 s[4:5], s[10:11], 19
	s_or_b32 s8, s16, s8
	s_lshl_b32 s11, s53, 5
	v_and_b32_e32 v176, 31, v86
	s_add_u32 s48, s8, s11
	v_or_b32_e32 v10, s48, v176
	s_movk_i32 s8, 0x600
	s_addc_u32 s49, s17, 0
	v_mad_u64_u32 v[2:3], s[16:17], v10, s8, v[2:3]
	v_bfe_u32 v186, v86, 5, 1
	v_mad_i32_i24 v3, s49, v177, v3
	s_mul_i32 s8, s87, 0xc0
	v_mov_b32_e32 v11, s49
	v_lshl_add_u64 v[2:3], v[2:3], 0, s[8:9]
	v_lshlrev_b32_e32 v178, 4, v186
	v_mov_b32_e32 v179, v175
	v_lshl_add_u64 v[26:27], v[2:3], 0, v[178:179]
	v_lshlrev_b64 v[10:11], 6, v[10:11]
	global_load_dwordx4 v[2:5], v[26:27], off offset:128
	global_load_dwordx4 v[6:9], v[26:27], off offset:160
	v_lshl_add_u64 v[12:13], s[12:13], 0, v[10:11]
	v_and_b32_e32 v174, 32, v86
	v_lshl_add_u64 v[10:11], s[14:15], 0, v[10:11]
	v_lshl_add_u64 v[22:23], v[12:13], 0, v[174:175]
	v_lshl_add_u64 v[18:19], v[10:11], 0, v[174:175]
	global_load_dwordx4 v[10:13], v[18:19], off
	global_load_dwordx4 v[14:17], v[22:23], off
	s_nop 0
	global_load_dwordx4 v[18:21], v[18:19], off offset:16
	s_nop 0
	global_load_dwordx4 v[22:25], v[22:23], off offset:16
	s_load_dwordx2 s[50:51], s[24:25], 0x1b0
	global_load_dwordx4 v[150:153], v[26:27], off
	global_load_dwordx4 v[138:141], v[26:27], off offset:32
	global_load_dwordx4 v[134:137], v[26:27], off offset:64
	global_load_dwordx4 v[130:133], v[26:27], off offset:96
	s_mul_hi_i32 s8, s10, 0xc0000
	s_mul_i32 s10, s10, 0xc0000
	s_add_u32 s10, s6, s10
	s_addc_u32 s11, s7, s8
	s_lshl_b32 s61, s53, 10
	s_add_i32 s96, s61, 0
	s_waitcnt lgkmcnt(0)
	s_add_u32 s4, s50, s4
	s_mov_b32 m0, s96
	v_lshlrev_b32_e32 v88, 6, v186
	s_addc_u32 s5, s51, s5
	s_add_i32 s97, s75, s61
	v_lshlrev_b32_e32 v90, 2, v86
	v_and_b32_e32 v91, 63, v86
	v_lshlrev_b32_e32 v93, 4, v91
	v_lshlrev_b32_e32 v92, 3, v91
	v_lshlrev_b32_e32 v94, 1, v91
	s_mov_b32 s8, s9
	s_mov_b32 s12, s9
	s_mov_b32 s13, s9
	s_mov_b32 s14, s9
	s_mov_b32 s15, s9
	s_mov_b32 s16, s9
	s_mov_b32 s17, s9
	s_mov_b32 s18, s9
	s_mov_b32 s19, s9
	s_mov_b32 s20, s9
	s_mov_b32 s21, s9
	s_mov_b32 s22, s9
	s_mov_b32 s23, s9
	s_mulk_i32 s53, 0x900
	v_mov_b32_e32 v83, v175
	v_mov_b32_e32 v85, v175
	v_and_b32_e32 v114, 28, v90
	v_lshl_add_u32 v187, v176, 2, s91
	v_mul_u32_u24_e32 v201, 0x44, v114
	v_bfe_u32 v195, v91, 1, 2
	v_mov_b32_e32 v207, 1.0
	s_mov_b32 s89, s9
	v_mov_b32_e32 v188, v175
	s_waitcnt vmcnt(9)
	v_lshlrev_b32_e32 v27, 16, v2
	s_waitcnt vmcnt(8)
	v_lshlrev_b32_e32 v26, 16, v6
	v_and_b32_e32 v33, 0xffff0000, v2
	v_lshlrev_b32_e32 v35, 16, v3
	s_waitcnt vmcnt(7)
	v_mov_b32_e32 v28, v10
	s_waitcnt vmcnt(6)
	v_mov_b32_e32 v29, v14
	v_mov_b32_e32 v36, v12
	v_mov_b32_e32 v37, v16
	v_mov_b32_e32 v38, v16
	v_mov_b32_e32 v39, v12
	v_and_b32_e32 v3, 0xffff0000, v3
	v_and_b32_e32 v2, 0xffff0000, v7
	v_mov_b32_e32 v16, v13
	v_mov_b32_e32 v12, v17
	v_and_b32_e32 v32, 0xffff0000, v6
	v_lshlrev_b32_e32 v34, 16, v7
	v_pk_mul_f32 v[6:7], v[28:29], v[26:27]
	v_pk_mul_f32 v[16:17], v[16:17], v[2:3]
	v_pk_mul_f32 v[2:3], v[12:13], v[2:3]
	v_mov_b32_e32 v30, v14
	v_mov_b32_e32 v31, v10
	v_sub_f32_e32 v12, v7, v6
	v_sub_f32_e32 v16, v17, v16
	v_add_f32_e32 v17, v2, v3
	v_lshlrev_b32_e32 v3, 16, v4
	v_lshlrev_b32_e32 v2, 16, v8
	s_waitcnt vmcnt(5)
	v_mov_b32_e32 v6, v18
	s_waitcnt vmcnt(4)
	v_mov_b32_e32 v7, v22
	v_pk_mul_f32 v[26:27], v[30:31], v[26:27]
	v_pk_mul_f32 v[6:7], v[6:7], v[2:3]
	v_add_f32_e32 v13, v26, v27
	v_sub_f32_e32 v26, v7, v6
	v_mov_b32_e32 v6, v22
	v_mov_b32_e32 v7, v18
	v_pk_mul_f32 v[2:3], v[6:7], v[2:3]
	v_mov_b32_e32 v22, v19
	v_add_f32_e32 v27, v2, v3
	v_and_b32_e32 v3, 0xffff0000, v4
	v_and_b32_e32 v2, 0xffff0000, v8
	v_mov_b32_e32 v18, v23
	v_pk_mul_f32 v[6:7], v[22:23], v[2:3]
	v_pk_mul_f32 v[2:3], v[18:19], v[2:3]
	v_sub_f32_e32 v8, v7, v6
	v_add_f32_e32 v18, v2, v3
	v_lshlrev_b32_e32 v3, 16, v5
	v_lshlrev_b32_e32 v2, 16, v9
	v_mov_b32_e32 v6, v20
	v_mov_b32_e32 v7, v24
	v_pk_mul_f32 v[6:7], v[6:7], v[2:3]
	v_mov_b32_e32 v14, v11
	v_sub_f32_e32 v19, v7, v6
	v_mov_b32_e32 v6, v24
	v_mov_b32_e32 v7, v20
	v_pk_mul_f32 v[2:3], v[6:7], v[2:3]
	v_mov_b32_e32 v24, v21
	v_add_f32_e32 v6, v2, v3
	v_and_b32_e32 v3, 0xffff0000, v5
	v_and_b32_e32 v2, 0xffff0000, v9
	v_mov_b32_e32 v20, v25
	v_mov_b32_e32 v10, v15
	v_pk_mul_f32 v[4:5], v[24:25], v[2:3]
	v_pk_mul_f32 v[2:3], v[20:21], v[2:3]
	v_pk_mul_f32 v[14:15], v[14:15], v[32:33]
	v_pk_mul_f32 v[10:11], v[10:11], v[32:33]
	v_pk_mul_f32 v[28:29], v[36:37], v[34:35]
	v_pk_mul_f32 v[30:31], v[38:39], v[34:35]
	v_add_f32_e32 v2, v2, v3
	v_sub_f32_e32 v14, v15, v14
	v_add_f32_e32 v10, v10, v11
	v_sub_f32_e32 v11, v29, v28
	v_add_f32_e32 v15, v30, v31
	v_sub_f32_e32 v4, v5, v4
	v_cvt_pk_bf16_f32 v146, v12, v14
	v_cvt_pk_bf16_f32 v142, v13, v10
	v_cvt_pk_bf16_f32 v147, v11, v16
	v_cvt_pk_bf16_f32 v143, v15, v17
	v_cvt_pk_bf16_f32 v148, v26, v8
	v_cvt_pk_bf16_f32 v144, v27, v18
	v_cvt_pk_bf16_f32 v149, v19, v4
	v_cvt_pk_bf16_f32 v145, v6, v2
	v_mul_u32_u24_e32 v2, 0xaaab, v86
	v_lshrrev_b32_e32 v3, 19, v2
	v_mul_lo_u16_e32 v4, 12, v3
	v_sub_u16_e32 v4, v86, v4
	v_lshrrev_b32_e32 v2, 21, v2
; #define LAS __attribute__((address_space(3)))
; DEVI int v_rd_base(int lane) { return ((lane & 3) << 3) | (((lane >> 2) & 3) << 6) | (((lane >> 4) & 1) << 5) | (((lane >> 5) & 1) << 8); }
; #define VM0() asm volatile("s_waitcnt vmcnt(0)" ::: "memory")
; DEVI void attn_unit8(const Params& p, char* smem, int unit, int l, int& cvs  , CvRun& crun) {
;     ...
;     int ksrc[3];
; #pragma unroll
;     for (int i = 0; i < 3; ++i) { const int pc = tid + 512 * i, row = pc / 12, ch = (pc % 12) ^ ((row >> 2) & 3); ksrc[i] = row * 192 + ch * 16; }
;     const int vsrc = wid * 1024 + ((lane >> 2) & 7) * 128 + (lane >> 5) * 64 + (lane & 3) * 16;
;     LAS char* const Kl = (LAS char*)K_lds + wid * 1024; LAS char* const Vl = (LAS char*)V_lds + wid * 1024;
;     ...
;     const int vb0 = (int)(uintptr_t)(LAS char*)V_lds + v_rd_base(lane);
;     float m_reg = 0.f, l_reg = 0.f; f32x16 o[2];
; #pragma unroll
;     for (int d = 0; d < 2; ++d)
; #pragma unroll
;         for (int r = 0; r < 16; ++r) o[d][r] = 0.f;
;     f32x16 pA0, pA1, pB0, pB1; float alA, alB; bf16x8 pa0, pa1, pa2, pa3;
;     constexpr int NTILE = S_ / 128;
;     B_DMA(0, 0); B_DMA(1, 1); VM0(); __syncthreads();
	v_bitop3_b32 v2, v2, v4, 3 bitop3:0x6c
	v_mul_u32_u24_e32 v3, 0xc0, v3
	v_lshl_add_u32 v174, v2, 4, v3
	v_or_b32_e32 v2, 0x200, v86
	v_mul_u32_u24_sdwa v3, v2, s74 dst_sel:DWORD dst_unused:UNUSED_PAD src0_sel:WORD_0 src1_sel:DWORD
	v_lshrrev_b32_e32 v4, 19, v3
	v_mul_lo_u16_e32 v5, 12, v4
	v_sub_u16_e32 v2, v2, v5
	v_lshrrev_b32_e32 v3, 21, v3
	v_bitop3_b32 v2, v3, v2, 3 bitop3:0x6c
	v_mul_u32_u24_e32 v3, 0xc0, v4
	v_lshl_add_u32 v82, v2, 4, v3
	v_or_b32_e32 v2, 0x400, v86
	v_mul_u32_u24_sdwa v3, v2, s74 dst_sel:DWORD dst_unused:UNUSED_PAD src0_sel:WORD_0 src1_sel:DWORD
	v_lshrrev_b32_e32 v4, 19, v3
	v_mul_lo_u16_e32 v5, 12, v4
	v_sub_u16_e32 v2, v2, v5
	v_lshrrev_b32_e32 v3, 21, v3
	v_bitop3_b32 v2, v3, v2, 3 bitop3:0x6c
	v_mul_u32_u24_e32 v3, 0xc0, v4
	v_lshl_add_u32 v84, v2, 4, v3
	v_lshlrev_b32_e32 v2, 5, v86
	v_and_b32_e32 v87, 0x380, v2
	v_lshlrev_b32_e32 v3, 4, v86
	global_load_lds_dwordx4 v174, s[10:11]
	s_add_i32 m0, s96, 0x2000
	v_or_b32_e32 v2, v88, v87
	v_and_b32_e32 v89, 48, v3
	global_load_lds_dwordx4 v82, s[10:11]
	s_add_i32 m0, s96, 0x4000
	v_or3_b32 v2, v2, v89, s61
	global_load_lds_dwordx4 v84, s[10:11]
	v_mov_b32_e32 v3, v175
	s_mov_b32 m0, s97
	v_lshl_add_u64 v[4:5], s[4:5], 0, v[2:3]
	global_load_lds_dwordx4 v2, s[4:5]
	s_add_i32 m0, s97, 0x2000
	v_lshl_add_u64 v[2:3], v[4:5], 0, s[40:41]
	s_add_u32 s4, s10, 0x6000
	global_load_lds_dwordx4 v[2:3], off
	s_addc_u32 s5, s11, 0
	s_add_i32 m0, s96, 0x6000
	v_lshl_add_u64 v[2:3], v[4:5], 0, s[44:45]
	global_load_lds_dwordx4 v174, s[4:5]
	s_add_i32 m0, s96, 0x8000
	v_mul_u32_u24_e32 v10, 0xc0, v176
	global_load_lds_dwordx4 v82, s[4:5]
	s_add_i32 m0, s96, 0xa000
	v_and_b32_e32 v11, 48, v90
	global_load_lds_dwordx4 v84, s[4:5]
	s_add_i32 m0, s97, 0x4000
	v_bitop3_b32 v129, v178, v10, v11 bitop3:0xde
	global_load_lds_dwordx4 v[2:3], off
	v_lshl_add_u64 v[2:3], v[4:5], 0, s[42:43]
	s_add_i32 m0, s97, 0x6000
	v_add_u32_e32 v189, 0, v129
	global_load_lds_dwordx4 v[2:3], off
	s_waitcnt vmcnt(0)
	s_waitcnt vmcnt(0) lgkmcnt(0)
	s_barrier
; #define VM0() asm volatile("s_waitcnt vmcnt(0)" ::: "memory")
; #define C_SPLAT() do { _Pragma("unroll") for (int _r = 0; _r < 16; ++_r) cinit[_r] = -m_reg; asm volatile("" : "+v"(cinit)); } while (0)
; template <bool FIRST> DEVI bool partialSM(f32x16& p0, f32x16& p1, float& m_reg, float& alpha) {
;     float pmax = p0[0];
; #pragma unroll
;     for (int r = 1; r < 16; ++r) pmax = fmaxf(pmax, p0[r]);
; #pragma unroll
;     for (int r = 0; r < 16; ++r) pmax = fmaxf(pmax, p1[r]);
;     { auto rr = __builtin_amdgcn_permlane32_swap(__float_as_uint(pmax), __float_as_uint(pmax), false, false);
;       pmax = fmaxf(__uint_as_float(rr[0]), __uint_as_float(rr[1])); }
;     if (FIRST) { m_reg = pmax; alpha = 1.f;
; #pragma unroll
;         for (int r = 0; r < 16; ++r) { p0[r] = __builtin_amdgcn_exp2f(p0[r] - pmax); p1[r] = p1[r] - pmax; }
;         return false;
; DEVI void attn_unit8(const Params& p, char* smem, int unit, int l, int& cvs  , CvRun& crun) {
;     ...
;     float m_reg = 0.f, l_reg = 0.f; f32x16 o[2];
; #pragma unroll
;     for (int d = 0; d < 2; ++d)
; #pragma unroll
;         for (int r = 0; r < 16; ++r) o[d][r] = 0.f;
;     f32x16 pA0, pA1, pB0, pB1; float alA, alB; bf16x8 pa0, pa1, pa2, pa3;
;     constexpr int NTILE = S_ / 128;
;     B_DMA(0, 0); B_DMA(1, 1); VM0(); __syncthreads();
;     f32x16 cinit;
;     ...
;     { f32x16 z; _Pragma("unroll") for (int r = 0; r < 16; ++r) z[r] = 0.f;
;       qkt(pA0, pA1, K_lds, qr, r32, hi, z); } partialSM<true>(pA0, pA1, m_reg, alA); C_SPLAT();
;     int s0 = 0, s1 = 1, s2 = 2;
	ds_read_b128 v[2:5], v189
	ds_read_b128 v[6:9], v189 offset:6144
	s_waitcnt lgkmcnt(1)
	v_mfma_f32_32x32x16_bf16 v[34:49], v[2:5], v[150:153], 0
	v_or_b32_e32 v2, 32, v178
	v_bitop3_b32 v184, v2, v10, v11 bitop3:0xde
	v_add_u32_e32 v190, 0, v184
	s_mov_b32 s10, s9
	s_mov_b32 s11, s9
	s_lshl_b32 s71, s54, 5
	s_lshl_b32 s84, s54, 4
	s_waitcnt lgkmcnt(0)
	v_mfma_f32_32x32x16_bf16 v[18:33], v[6:9], v[150:153], 0
	ds_read_b128 v[2:5], v190
	ds_read_b128 v[6:9], v190 offset:6144
	s_lshl_b32 s85, s54, 3
	s_lshl_b32 s88, s54, 1
	v_cmp_gt_u32_e64 s[4:5], 32, v91
	s_waitcnt lgkmcnt(1)
	v_mfma_f32_32x32x16_bf16 v[34:49], v[2:5], v[138:141], v[34:49]
	v_or_b32_e32 v2, 64, v178
	v_xad_u32 v185, v2, v11, v10
	v_add_u32_e32 v191, 0, v185
	s_waitcnt lgkmcnt(0)
	v_mfma_f32_32x32x16_bf16 v[18:33], v[6:9], v[138:141], v[18:33]
	ds_read_b128 v[2:5], v191
	ds_read_b128 v[6:9], v191 offset:6144
	s_waitcnt lgkmcnt(1)
	v_mfma_f32_32x32x16_bf16 v[34:49], v[2:5], v[134:137], v[34:49]
	v_or_b32_e32 v2, 0x60, v178
	v_xad_u32 v204, v2, v11, v10
	v_add_u32_e32 v192, 0, v204
	ds_read_b128 v[2:5], v192
	s_waitcnt lgkmcnt(1)
	v_mfma_f32_32x32x16_bf16 v[18:33], v[6:9], v[134:137], v[18:33]
	ds_read_b128 v[6:9], v192 offset:6144
	s_waitcnt lgkmcnt(1)
	v_mfma_f32_32x32x16_bf16 v[34:49], v[2:5], v[130:133], v[34:49]
	v_and_b32_e32 v2, 0xc0, v93
	v_and_or_b32 v12, v92, 24, v2
	v_or_b32_e32 v2, 0x80, v178
	v_xad_u32 v205, v2, v11, v10
	v_add_u32_e32 v193, 0, v205
	ds_read_b128 v[2:5], v193
	s_waitcnt lgkmcnt(1)
	v_mfma_f32_32x32x16_bf16 v[18:33], v[6:9], v[130:133], v[18:33]
	v_and_b32_e32 v6, 32, v94
	v_and_b32_e32 v7, 0x100, v92
	v_or3_b32 v179, v12, v6, v7
	ds_read_b128 v[6:9], v193 offset:6144
	v_add_u32_e32 v115, s75, v179
	s_waitcnt lgkmcnt(1)
	v_mfma_f32_32x32x16_bf16 v[34:49], v[2:5], v[146:149], v[34:49]
	v_or_b32_e32 v2, 0xa0, v178
	v_xad_u32 v206, v2, v11, v10
	v_add_u32_e32 v194, 0, v206
	ds_read_b128 v[2:5], v194
	ds_read_b128 v[50:53], v194 offset:6144
	s_waitcnt lgkmcnt(2)
	v_mfma_f32_32x32x16_bf16 v[18:33], v[6:9], v[146:149], v[18:33]
	s_waitcnt lgkmcnt(1)
	v_mfma_f32_32x32x16_bf16 v[34:49], v[2:5], v[142:145], v[34:49]
	v_mov_b64_e32 v[2:3], s[8:9]
	v_mov_b64_e32 v[4:5], s[10:11]
	v_mov_b64_e32 v[6:7], s[12:13]
	v_mov_b64_e32 v[8:9], s[14:15]
	v_mov_b64_e32 v[10:11], s[16:17]
	v_mov_b64_e32 v[12:13], s[18:19]
	v_mov_b64_e32 v[14:15], s[20:21]
	s_waitcnt lgkmcnt(0)
	v_mfma_f32_32x32x16_bf16 v[18:33], v[50:53], v[142:145], v[18:33]
	s_nop 2
	v_max_f32_e32 v50, v35, v35
	v_max_f32_e32 v51, v34, v34
	v_max_f32_e32 v50, v51, v50
	v_max3_f32 v50, v50, v36, v37
	v_max3_f32 v50, v50, v38, v39
	v_max3_f32 v50, v50, v40, v41
	v_max3_f32 v50, v50, v42, v43
	v_max3_f32 v50, v50, v44, v45
	v_max3_f32 v50, v50, v46, v47
	v_max3_f32 v50, v50, v48, v49
	v_max3_f32 v50, v50, v18, v19
	v_max3_f32 v50, v50, v20, v21
	v_max3_f32 v50, v50, v22, v23
	v_max3_f32 v50, v50, v24, v25
	v_max3_f32 v50, v50, v26, v27
	v_max3_f32 v50, v50, v28, v29
	v_max3_f32 v50, v50, v30, v31
	v_max3_f32 v50, v50, v32, v33
	v_mov_b32_e32 v51, v50
	s_nop 1
	v_permlane32_swap_b32_e32 v50, v51
	v_max_f32_e32 v51, v51, v51
	v_max_f32_e32 v50, v50, v50
	v_max_f32_e32 v203, v50, v51
	v_sub_f32_e32 v34, v34, v203
	v_exp_f32_e32 v50, v34
	v_sub_f32_e32 v34, v35, v203
	v_exp_f32_e32 v51, v34
	v_sub_f32_e32 v34, v36, v203
	v_exp_f32_e32 v52, v34
	v_sub_f32_e32 v34, v37, v203
	v_exp_f32_e32 v53, v34
	v_sub_f32_e32 v34, v38, v203
	v_exp_f32_e32 v54, v34
	v_sub_f32_e32 v34, v39, v203
	v_exp_f32_e32 v55, v34
	v_sub_f32_e32 v34, v40, v203
	v_exp_f32_e32 v56, v34
	v_sub_f32_e32 v34, v41, v203
	v_exp_f32_e32 v57, v34
	v_sub_f32_e32 v34, v42, v203
	v_mov_b64_e32 v[16:17], s[22:23]
	v_exp_f32_e32 v58, v34
	v_sub_f32_e32 v34, v43, v203
	v_sub_f32_e32 v67, v19, v203
	s_add_i32 s8, s53, 0
	v_bfe_u32 v19, v86, 1, 5
	v_exp_f32_e32 v59, v34
	v_sub_f32_e32 v34, v44, v203
	v_sub_f32_e32 v68, v20, v203
	s_add_i32 s8, s8, 0x1e800
	v_and_b32_e32 v20, 28, v19
	s_or_b32 s10, s52, s2
	v_exp_f32_e32 v60, v34
	v_sub_f32_e32 v34, v45, v203
	v_sub_f32_e32 v69, v21, v203
	v_add_u32_e32 v200, s8, v20
	v_mov_b32_e32 v21, s8
	s_lshl_b32 s8, s54, 10
	s_ashr_i32 s11, s10, 31
	v_exp_f32_e32 v61, v34
	v_sub_f32_e32 v34, v46, v203
	s_add_i32 s70, s8, 0xf7f80000
	s_lshl_b64 s[12:13], s[10:11], 19
	v_exp_f32_e32 v62, v34
	v_sub_f32_e32 v34, v47, v203
	v_sub_f32_e32 v66, v18, v203
	v_lshrrev_b32_e32 v18, 2, v86
	s_add_u32 s12, s50, s12
	v_exp_f32_e32 v63, v34
	v_sub_f32_e32 v34, v48, v203
	v_sub_f32_e32 v70, v22, v203
	v_and_b32_e32 v128, 14, v18
	v_lshrrev_b32_e32 v22, 3, v86
	v_and_b32_e32 v18, 12, v18
	s_addc_u32 s13, s51, s13
	s_mul_i32 s8, s10, 0xc0000
	v_exp_f32_e32 v64, v34
	v_sub_f32_e32 v34, v49, v203
	v_mad_u32_u24 v198, v19, s77, v21
	v_and_b32_e32 v19, 0x80, v92
	v_and_b32_e32 v21, 16, v94
	v_and_b32_e32 v22, 4, v22
	v_and_or_b32 v197, v93, s76, v18
	v_or_b32_e32 v18, s61, v87
	s_mul_hi_i32 s2, s10, 0xc0000
	s_add_u32 s6, s6, s8
	v_exp_f32_e32 v65, v34
	v_or3_b32 v196, v19, v22, v21
	v_or3_b32 v18, v18, v88, v89
	v_mov_b32_e32 v19, v175
	s_addc_u32 s2, s7, s2
	v_and_b32_e32 v20, 1, v86

; #define LAS __attribute__((address_space(3)))
; DEVI int v_rd_base(int lane) { return ((lane & 3) << 3) | (((lane >> 2) & 3) << 6) | (((lane >> 4) & 1) << 5) | (((lane >> 5) & 1) << 8); }
; #define VM0() asm volatile("s_waitcnt vmcnt(0)" ::: "memory")
; #define C_SPLAT() do { _Pragma("unroll") for (int _r = 0; _r < 16; ++_r) cinit[_r] = -m_reg; asm volatile("" : "+v"(cinit)); } while (0)
; DEVI void attn_unit8(const Params& p, char* smem, int unit, int l, int& cvs  , CvRun& crun) {
;     ...
;     const int vsrc = wid * 1024 + ((lane >> 2) & 7) * 128 + (lane >> 5) * 64 + (lane & 3) * 16;
;     LAS char* const Kl = (LAS char*)K_lds + wid * 1024; LAS char* const Vl = (LAS char*)V_lds + wid * 1024;
;     ...
;     const int vb0 = (int)(uintptr_t)(LAS char*)V_lds + v_rd_base(lane);
;     float m_reg = 0.f, l_reg = 0.f; f32x16 o[2];
; #pragma unroll
;     for (int d = 0; d < 2; ++d)
; #pragma unroll
;         for (int r = 0; r < 16; ++r) o[d][r] = 0.f;
;     f32x16 pA0, pA1, pB0, pB1; float alA, alB; bf16x8 pa0, pa1, pa2, pa3;
;     constexpr int NTILE = S_ / 128;
;     B_DMA(0, 0); B_DMA(1, 1); VM0(); __syncthreads();
;     f32x16 cinit;
;     ...
;     { f32x16 z; _Pragma("unroll") for (int r = 0; r < 16; ++r) z[r] = 0.f;
;       qkt(pA0, pA1, K_lds, qr, r32, hi, z); } partialSM<true>(pA0, pA1, m_reg, alA); C_SPLAT();
;     int s0 = 0, s1 = 1, s2 = 2;
	s_add_u32 s6, s6, 0xc000
	v_xor_b32_e32 v34, 0x80000000, v203
	v_sub_f32_e32 v81, v33, v203
	v_sub_f32_e32 v80, v32, v203
	v_sub_f32_e32 v79, v31, v203
	v_sub_f32_e32 v78, v30, v203
	v_sub_f32_e32 v77, v29, v203
	v_sub_f32_e32 v76, v28, v203
	v_sub_f32_e32 v75, v27, v203
	v_sub_f32_e32 v74, v26, v203
	v_sub_f32_e32 v73, v25, v203
	v_sub_f32_e32 v72, v24, v203
	v_sub_f32_e32 v71, v23, v203
	v_lshlrev_b32_e32 v199, 5, v20
	v_lshlrev_b32_e32 v180, 4, v20
	v_mov_b32_e32 v116, v18
	v_add_u32_e32 v117, 0x2000, v18
	s_addc_u32 s7, s2, 0
	s_add_u32 s44, s12, 0x8000
	s_addc_u32 s45, s13, 0
	v_mov_b64_e32 v[32:33], v[16:17]
	v_mov_b32_e32 v35, v34
	v_mov_b32_e32 v36, v34
	v_mov_b32_e32 v37, v34
	v_mov_b32_e32 v38, v34
	v_mov_b32_e32 v39, v34
	v_mov_b32_e32 v40, v34
	v_mov_b32_e32 v41, v34
	v_mov_b32_e32 v42, v34
	v_mov_b32_e32 v43, v34
	v_mov_b32_e32 v44, v34
	v_mov_b32_e32 v45, v34
	v_mov_b32_e32 v46, v34
	v_mov_b32_e32 v47, v34
	v_mov_b32_e32 v48, v34
	v_mov_b32_e32 v49, v34
	v_mov_b32_e32 v118, v174
	v_mov_b32_e32 v120, v82
	v_mov_b32_e32 v122, v84
	s_mov_b64 s[12:13], s[6:7]
	s_add_u32 s67, s6, 0xb4000
	v_mov_b64_e32 v[30:31], v[14:15]
	v_mov_b64_e32 v[28:29], v[12:13]
	v_mov_b64_e32 v[26:27], v[10:11]
	v_mov_b64_e32 v[24:25], v[8:9]
	v_mov_b64_e32 v[22:23], v[6:7]
	v_mov_b64_e32 v[20:21], v[4:5]
	v_mov_b64_e32 v[18:19], v[2:3]
	s_mov_b32 s6, 2
	s_mov_b32 s2, 1

; #define VM0() asm volatile("s_waitcnt vmcnt(0)" ::: "memory")
; #define B_RESC(a, rare) do { if (rare) { if (hi == 0) al_l[r32] = (a); asm volatile("s_waitcnt lgkmcnt(0)" ::: "memory"); __builtin_amdgcn_wave_barrier(); \
;         _Pragma("unroll") for (int _d = 0; _d < 2; ++_d) _Pragma("unroll") for (int _r = 0; _r < 16; ++_r) o[_d][_r] *= al_l[crow(_r, hi)]; C_SPLAT(); } } while (0)
; DEVI void attn_unit8(const Params& p, char* smem, int unit, int l, int& cvs  , CvRun& crun) {
;     ...
;     for (int T = 0; T + 1 < NTILE; ++T) {
;         const char* Kb = K_lds + s0 * 24576; const int vb = vb0 + s0 * 16384;
;         CvRegs cvr; cv_issue(p, l, cvs, lane, cvr, crun); cvs += (int)gridDim.x * 8;
;         qkt(pB0, pB1, Kb + 12288, qr, r32, hi, cinit);
;         finishSM(pA0, pA1, alA, l_reg, pa0, pa1, pa2, pa3);
;         pv_both(o[0], o[1], vb, pa0, pa1, pa2, pa3);
;         { const bool rr_ = partialSM<false>(pB0, pB1, m_reg, alB); B_RESC(alB, rr_); }
;         cv_finish(smem + 124928 + wid * 2304, lane, cvr);
;         if (cvr.live) asm volatile("s_waitcnt vmcnt(2)" ::: "memory"); else VM0();
;         __syncthreads();
;         if (T + 2 < NTILE) B_DMA(T + 2, s2);
.LBB0_702:
	s_mul_i32 s98, s2, 0x6000
	s_add_i32 s98, s96, s98
	s_lshl_b32 s99, s2, 14
	s_add_i32 s99, s97, s99
	s_mul_i32 s6, s61, 0x6000
	s_add_i32 s6, s6, 0
	v_add_u32_e32 v249, s6, v129

; #define VM0() asm volatile("s_waitcnt vmcnt(0)" ::: "memory")
; DEVI void attn_unit8(const Params& p, char* smem, int unit, int l, int& cvs  , CvRun& crun) {
;     ...
;         if (cvr.live) asm volatile("s_waitcnt vmcnt(2)" ::: "memory"); else VM0();
;         __syncthreads();
;         if (T + 2 < NTILE) B_DMA(T + 2, s2);
;         qkt(pA0, pA1, K_lds + s1 * 24576, qr, r32, hi, cinit);
	s_mov_b32 m0, s98
	s_barrier
	ds_read_b128 v[234:237], v249
	ds_read_b128 v[210:213], v249 offset:6144
	global_load_lds_dwordx4 v118, s[12:13]
	s_waitcnt lgkmcnt(1)
	v_mfma_f32_32x32x16_bf16 v[98:113], v[234:237], v[150:153], v[34:49]
	s_add_i32 m0, s98, 0x2000

; DEVI void attn_unit8(const Params& p, char* smem, int unit, int l, int& cvs  , CvRun& crun) {
;     ...
;         if (T + 2 < NTILE) B_DMA(T + 2, s2);
;         qkt(pA0, pA1, K_lds + s1 * 24576, qr, r32, hi, cinit);
	v_add_u32_e32 v126, s6, v184
	global_load_lds_dwordx4 v120, s[12:13]
	s_waitcnt lgkmcnt(0)
	v_mfma_f32_32x32x16_bf16 v[66:81], v[210:213], v[150:153], v[34:49]
	ds_read_b128 v[210:213], v126
	ds_read_b128 v[214:217], v126 offset:6144
	s_add_i32 m0, s98, 0x4000

; #define PK4(P, BASE, OUT) do { u32x4 w = {cvt_pk_bf16(P[BASE + 0], P[BASE + 1]), cvt_pk_bf16(P[BASE + 2], P[BASE + 3]), cvt_pk_bf16(P[BASE + 4], P[BASE + 5]), cvt_pk_bf16(P[BASE + 6], P[BASE + 7])}; \
;     OUT = *reinterpret_cast<bf16x8*>(&w); } while (0)
; DEVI void finishSM(f32x16& p0, f32x16& p1, float alpha, float& l_reg, bf16x8& pa0, bf16x8& pa1, bf16x8& pa2, bf16x8& pa3) {
; #pragma unroll
;     for (int r = 0; r < 16; ++r) p1[r] = __builtin_amdgcn_exp2f(p1[r]);
;     f32x2 s2 = (f32x2){p0[0], p0[1]} + (f32x2){p1[0], p1[1]};
; #pragma unroll
;     for (int r = 2; r < 16; r += 2) s2 += (f32x2){p0[r], p0[r + 1]} + (f32x2){p1[r], p1[r + 1]};
;     float ps = s2[0] + s2[1];
;     { auto rr = __builtin_amdgcn_permlane32_swap(__float_as_uint(ps), __float_as_uint(ps), false, false);
;       ps = __uint_as_float(rr[0]) + __uint_as_float(rr[1]); }
;     l_reg = l_reg * alpha + ps;
;     ...
;     PK4(p0, 0, pa0); PK4(p0, 8, pa1); PK4(p1, 0, pa2); PK4(p1, 8, pa3);
;     ...
; }
; DEVI void qkt(f32x16& p0, f32x16& p1, const char* Kb, const bf16x8 (&qr)[6], int r32, int hi, const f32x16& cinit) {
; #pragma unroll
;     for (int d0 = 0; d0 < 6; ++d0) { const int cb = (d0 * 16 + hi * 8) * 2;
;         const bf16x8 k0 = *(const bf16x8*)(Kb + KSWZ(r32, cb)), k1 = *(const bf16x8*)(Kb + KSWZ(32 + r32, cb));
;         p0 = __builtin_amdgcn_mfma_f32_32x32x16_bf16(k0, qr[d0], d0 == 0 ? cinit : p0, 0, 0, 0);
;         p1 = __builtin_amdgcn_mfma_f32_32x32x16_bf16(k1, qr[d0], d0 == 0 ? cinit : p1, 0, 0, 0); }
; }
	v_add_u32_e32 v126, s6, v185
	global_load_lds_dwordx4 v122, s[12:13]
	s_waitcnt lgkmcnt(1)
	v_mfma_f32_32x32x16_bf16 v[98:113], v[210:213], v[138:141], v[98:113]
	s_mov_b32 m0, s99
	s_nop 0
	global_load_lds_dwordx4 v116, s[44:45]
	s_add_i32 m0, s99, 0x2000
	v_add_u32_e32 v174, 0x2000, v202
	global_load_lds_dwordx4 v117, s[44:45]
	s_waitcnt lgkmcnt(0)
	v_mfma_f32_32x32x16_bf16 v[66:81], v[214:217], v[138:141], v[66:81]
	ds_read_b128 v[210:213], v126
	ds_read_b128 v[214:217], v126 offset:6144
	v_add_u32_e32 v126, s6, v204
	s_waitcnt lgkmcnt(1)
	v_mfma_f32_32x32x16_bf16 v[98:113], v[210:213], v[134:137], v[98:113]
	ds_read_b128 v[210:213], v126
	ds_read_b128 v[218:221], v126 offset:6144
	v_add_u32_e32 v126, s6, v205
	s_waitcnt lgkmcnt(2)
	v_mfma_f32_32x32x16_bf16 v[66:81], v[214:217], v[134:137], v[66:81]
	ds_read_b128 v[214:217], v126
	ds_read_b128 v[222:225], v126 offset:6144
	v_add_u32_e32 v126, s6, v206
	ds_read_b128 v[226:229], v126
	ds_read_b128 v[230:233], v126 offset:6144
	v_add_f32_e32 v126, v50, v82
	v_add_f32_e32 v127, v51, v83
	v_cvt_pk_bf16_f32 v50, v50, v51
	v_cvt_pk_bf16_f32 v51, v52, v53
	s_waitcnt lgkmcnt(5)
	v_mfma_f32_32x32x16_bf16 v[98:113], v[210:213], v[130:133], v[98:113]
	v_add_f32_e64 v210, v52, v84
	v_add_f32_e64 v211, v53, v85
	v_cvt_pk_bf16_f32 v52, v54, v55
	v_cvt_pk_bf16_f32 v53, v56, v57
	v_add_f32_e64 v126, v210, v126
	v_add_f32_e64 v127, v211, v127
	v_add_f32_e64 v210, v54, v86
	v_add_f32_e64 v211, v55, v87
	v_cvt_pk_bf16_f32 v54, v58, v59
	s_waitcnt lgkmcnt(4)
	v_mfma_f32_32x32x16_bf16 v[66:81], v[218:221], v[130:133], v[66:81]
	v_add_f32_e64 v126, v210, v126
	v_add_f32_e64 v127, v211, v127
	v_add_f32_e64 v210, v56, v88
	v_add_f32_e64 v211, v57, v89
	v_cvt_pk_bf16_f32 v55, v60, v61
	v_cvt_pk_bf16_f32 v56, v62, v63
	v_cvt_pk_bf16_f32 v57, v64, v65
	v_add_f32_e64 v126, v210, v126
	v_add_f32_e64 v127, v211, v127
	v_add_f32_e32 v210, v58, v90
	v_add_f32_e32 v211, v59, v91
	v_cvt_pk_bf16_f32 v58, v82, v83
	v_cvt_pk_bf16_f32 v59, v84, v85
	s_waitcnt lgkmcnt(3)
	v_mfma_f32_32x32x16_bf16 v[98:113], v[214:217], v[146:149], v[98:113]
	v_add_f32_e64 v126, v210, v126
	v_add_f32_e64 v127, v211, v127
	v_add_f32_e64 v210, v60, v92
	v_add_f32_e64 v211, v61, v93
	v_cvt_pk_bf16_f32 v60, v86, v87
	v_cvt_pk_bf16_f32 v61, v88, v89
	v_add_f32_e64 v126, v210, v126
	v_add_f32_e64 v127, v211, v127
	v_add_f32_e32 v210, v62, v94
	v_add_f32_e32 v211, v63, v95
	v_cvt_pk_bf16_f32 v62, v90, v91
	v_cvt_pk_bf16_f32 v63, v92, v93
	s_waitcnt lgkmcnt(2)
	v_mfma_f32_32x32x16_bf16 v[66:81], v[222:225], v[146:149], v[66:81]
	v_add_f32_e64 v126, v210, v126
	v_add_f32_e64 v127, v211, v127
	v_add_f32_e64 v210, v64, v96
	v_add_f32_e64 v211, v65, v97
	v_cvt_pk_bf16_f32 v64, v94, v95
	v_cvt_pk_bf16_f32 v65, v96, v97
	ds_read_b64_tr_b16 v[154:155], v174 offset:0
	ds_read_b64_tr_b16 v[156:157], v174 offset:0x400
	ds_read_b64_tr_b16 v[158:159], v174 offset:0x800
	ds_read_b64_tr_b16 v[160:161], v174 offset:0xc00
	ds_read_b64_tr_b16 v[162:163], v174 offset:0x1000
	ds_read_b64_tr_b16 v[164:165], v174 offset:0x1400
	ds_read_b64_tr_b16 v[166:167], v174 offset:0x1800
	ds_read_b64_tr_b16 v[168:169], v174 offset:0x1c00
	v_add_f32_e64 v126, v210, v126
	v_add_f32_e64 v127, v211, v127
	ds_read_b64_tr_b16 v[210:211], v174 offset:0x200
	ds_read_b64_tr_b16 v[212:213], v174 offset:0x600
	ds_read_b64_tr_b16 v[214:215], v174 offset:0xa00
	s_waitcnt lgkmcnt(12)
	v_mfma_f32_32x32x16_bf16 v[98:113], v[226:229], v[142:145], v[98:113]
	ds_read_b64_tr_b16 v[216:217], v174 offset:0xe00
	ds_read_b64_tr_b16 v[218:219], v174 offset:0x1200
	ds_read_b64_tr_b16 v[220:221], v174 offset:0x1600
	ds_read_b64_tr_b16 v[222:223], v174 offset:0x1a00
	ds_read_b64_tr_b16 v[224:225], v174 offset:0x1e00
	v_add_f32_e32 v126, v126, v127
	s_waitcnt lgkmcnt(15)
	v_mfma_f32_32x32x16_bf16 v[66:81], v[230:233], v[142:145], v[66:81]
	v_mov_b32_e32 v127, v126


; DEVI void pv_both(f32x16& o0, f32x16& o1, int vb, bf16x8 pa0, bf16x8 pa1, bf16x8 pa2, bf16x8 pa3) {
;     const s16x4 a0 = tr_read<v_rd_off(0, 0, 0)>(vb), b0 = tr_read<v_rd_off(0, 0, 1)>(vb), a1 = tr_read<v_rd_off(0, 1, 0)>(vb), b1 = tr_read<v_rd_off(0, 1, 1)>(vb);
;     const s16x4 a2 = tr_read<v_rd_off(0, 2, 0)>(vb), b2 = tr_read<v_rd_off(0, 2, 1)>(vb), a3 = tr_read<v_rd_off(0, 3, 0)>(vb), b3 = tr_read<v_rd_off(0, 3, 1)>(vb);
;     const s16x4 c0 = tr_read<v_rd_off(1, 0, 0)>(vb), d0 = tr_read<v_rd_off(1, 0, 1)>(vb), c1 = tr_read<v_rd_off(1, 1, 0)>(vb), d1 = tr_read<v_rd_off(1, 1, 1)>(vb);
;     const s16x4 c2 = tr_read<v_rd_off(1, 2, 0)>(vb), d2 = tr_read<v_rd_off(1, 2, 1)>(vb), c3 = tr_read<v_rd_off(1, 3, 0)>(vb), d3 = tr_read<v_rd_off(1, 3, 1)>(vb);
;     asm volatile("s_waitcnt lgkmcnt(8)" ::: "memory"); SBAR();
;     ...
;     o0 = __builtin_amdgcn_mfma_f32_32x32x16_bf16(pa0, PK(a0, b0), o0, 0, 0, 0);
;     o0 = __builtin_amdgcn_mfma_f32_32x32x16_bf16(pa1, PK(a1, b1), o0, 0, 0, 0);
;     o0 = __builtin_amdgcn_mfma_f32_32x32x16_bf16(pa2, PK(a2, b2), o0, 0, 0, 0);
;     o0 = __builtin_amdgcn_mfma_f32_32x32x16_bf16(pa3, PK(a3, b3), o0, 0, 0, 0);
;     asm volatile("s_waitcnt lgkmcnt(0)" ::: "memory"); SBAR();
;     o1 = __builtin_amdgcn_mfma_f32_32x32x16_bf16(pa0, PK(c0, d0), o1, 0, 0, 0);
;     o1 = __builtin_amdgcn_mfma_f32_32x32x16_bf16(pa1, PK(c1, d1), o1, 0, 0, 0);
;     o1 = __builtin_amdgcn_mfma_f32_32x32x16_bf16(pa2, PK(c2, d2), o1, 0, 0, 0);
;     o1 = __builtin_amdgcn_mfma_f32_32x32x16_bf16(pa3, PK(c3, d3), o1, 0, 0, 0);
;     ...
; }
; template <bool FIRST> DEVI bool partialSM(f32x16& p0, f32x16& p1, float& m_reg, float& alpha) {
;     float pmax = p0[0];
; #pragma unroll
;     for (int r = 1; r < 16; ++r) pmax = fmaxf(pmax, p0[r]);
; #pragma unroll
;     for (int r = 0; r < 16; ++r) pmax = fmaxf(pmax, p1[r]);
;     { auto rr = __builtin_amdgcn_permlane32_swap(__float_as_uint(pmax), __float_as_uint(pmax), false, false);
;       pmax = fmaxf(__uint_as_float(rr[0]), __uint_as_float(rr[1])); }
;     if (FIRST) { m_reg = pmax; alpha = 1.f;
; #pragma unroll
;         for (int r = 0; r < 16; ++r) { p0[r] = __builtin_amdgcn_exp2f(p0[r] - pmax); p1[r] = p1[r] - pmax; }
;         return false;
;     } else if (__builtin_expect(__all(pmax <= ATT_THR), 1)) { alpha = 1.f;
; #pragma unroll
;         for (int r = 0; r < 16; ++r) p0[r] = __builtin_amdgcn_exp2f(p0[r]);
	s_waitcnt lgkmcnt(14)
	v_mfma_f32_32x32x16_bf16 v[18:33], v[50:53], v[154:157], v[18:33]
	v_permlane32_swap_b32_e32 v126, v127
	s_waitcnt lgkmcnt(6)
	v_mfma_f32_32x32x16_bf16 v[2:17], v[50:53], v[210:213], v[2:17]
	s_nop 1
	v_max_f32_e32 v249, v99, v99
	v_max_f32_e32 v250, v98, v98
	v_max_f32_e32 v249, v250, v249
	v_max3_f32 v249, v249, v100, v101
	v_max3_f32 v249, v249, v102, v103
	v_max3_f32 v251, v249, v104, v105
	v_max3_f32 v251, v251, v106, v107
	v_exp_f32_e32 v50, v98
	v_exp_f32_e32 v51, v99
	v_exp_f32_e32 v52, v100
	v_exp_f32_e32 v53, v101
	v_mfma_f32_32x32x16_bf16 v[18:33], v[54:57], v[158:161], v[18:33]
	s_waitcnt lgkmcnt(4)
	v_mfma_f32_32x32x16_bf16 v[2:17], v[54:57], v[214:217], v[2:17]
	v_max3_f32 v251, v251, v108, v109
	v_max3_f32 v251, v251, v110, v111
	v_max3_f32 v251, v251, v112, v113
	v_max3_f32 v251, v251, v66, v67
	v_max3_f32 v251, v251, v68, v69
	v_max3_f32 v251, v251, v70, v71
	v_max3_f32 v251, v251, v72, v73
	v_exp_f32_e32 v54, v102
	v_exp_f32_e32 v55, v103
	v_exp_f32_e32 v56, v104
	v_exp_f32_e32 v57, v105
	v_mfma_f32_32x32x16_bf16 v[18:33], v[58:61], v[162:165], v[18:33]
	s_waitcnt lgkmcnt(2)
	v_mfma_f32_32x32x16_bf16 v[2:17], v[58:61], v[218:221], v[2:17]
	v_max3_f32 v251, v251, v74, v75
	v_max3_f32 v251, v251, v76, v77
	v_max3_f32 v251, v251, v78, v79
	v_max3_f32 v251, v251, v80, v81
	v_mov_b32_e32 v252, v251


; #define SBAR() __builtin_amdgcn_sched_barrier(0)
; DEVI void pv_both(f32x16& o0, f32x16& o1, int vb, bf16x8 pa0, bf16x8 pa1, bf16x8 pa2, bf16x8 pa3) {
;     ...
;     o0 = __builtin_amdgcn_mfma_f32_32x32x16_bf16(pa0, PK(a0, b0), o0, 0, 0, 0);
;     o0 = __builtin_amdgcn_mfma_f32_32x32x16_bf16(pa1, PK(a1, b1), o0, 0, 0, 0);
;     o0 = __builtin_amdgcn_mfma_f32_32x32x16_bf16(pa2, PK(a2, b2), o0, 0, 0, 0);
;     o0 = __builtin_amdgcn_mfma_f32_32x32x16_bf16(pa3, PK(a3, b3), o0, 0, 0, 0);
;     asm volatile("s_waitcnt lgkmcnt(0)" ::: "memory"); SBAR();
;     o1 = __builtin_amdgcn_mfma_f32_32x32x16_bf16(pa0, PK(c0, d0), o1, 0, 0, 0);
;     o1 = __builtin_amdgcn_mfma_f32_32x32x16_bf16(pa1, PK(c1, d1), o1, 0, 0, 0);
;     o1 = __builtin_amdgcn_mfma_f32_32x32x16_bf16(pa2, PK(c2, d2), o1, 0, 0, 0);
;     o1 = __builtin_amdgcn_mfma_f32_32x32x16_bf16(pa3, PK(c3, d3), o1, 0, 0, 0);
; template <bool FIRST> DEVI bool partialSM(f32x16& p0, f32x16& p1, float& m_reg, float& alpha) {
;     float pmax = p0[0];
; #pragma unroll
;     for (int r = 1; r < 16; ++r) pmax = fmaxf(pmax, p0[r]);
; #pragma unroll
;     for (int r = 0; r < 16; ++r) pmax = fmaxf(pmax, p1[r]);
;     { auto rr = __builtin_amdgcn_permlane32_swap(__float_as_uint(pmax), __float_as_uint(pmax), false, false);
;       pmax = fmaxf(__uint_as_float(rr[0]), __uint_as_float(rr[1])); }
;     if (FIRST) { m_reg = pmax; alpha = 1.f;
; #pragma unroll
;         for (int r = 0; r < 16; ++r) { p0[r] = __builtin_amdgcn_exp2f(p0[r] - pmax); p1[r] = p1[r] - pmax; }
;         return false;
;     } else if (__builtin_expect(__all(pmax <= ATT_THR), 1)) { alpha = 1.f;
; #pragma unroll
;         for (int r = 0; r < 16; ++r) p0[r] = __builtin_amdgcn_exp2f(p0[r]);
	v_exp_f32_e32 v58, v106
	v_exp_f32_e32 v59, v107
	v_permlane32_swap_b32_e32 v251, v252
	v_exp_f32_e32 v60, v108
	v_exp_f32_e32 v61, v109
	v_mfma_f32_32x32x16_bf16 v[18:33], v[62:65], v[166:169], v[18:33]
	s_waitcnt lgkmcnt(0)
	v_mfma_f32_32x32x16_bf16 v[2:17], v[62:65], v[222:225], v[2:17]
	v_exp_f32_e32 v62, v110
	v_exp_f32_e32 v63, v111
	v_exp_f32_e32 v64, v112
	v_exp_f32_e32 v65, v113
	v_max_f32_e32 v252, v252, v252
	v_max_f32_e32 v251, v251, v251
	v_max_f32_e32 v174, v251, v252
	v_cmp_ge_f32_e32 vcc, s79, v174
	s_cmp_lg_u64 vcc, exec
	s_cselect_b64 s[6:7], -1, 0
	s_cbranch_scc1 .LBB0_711
	v_mov_b32_e32 v202, 1.0
	v_mov_b32_e32 v203, v209
	s_branch .LBB0_716

; #define VM0() asm volatile("s_waitcnt vmcnt(0)" ::: "memory")
; #define B_RESC(a, rare) do { if (rare) { if (hi == 0) al_l[r32] = (a); asm volatile("s_waitcnt lgkmcnt(0)" ::: "memory"); __builtin_amdgcn_wave_barrier(); \
;         _Pragma("unroll") for (int _d = 0; _d < 2; ++_d) _Pragma("unroll") for (int _r = 0; _r < 16; ++_r) o[_d][_r] *= al_l[crow(_r, hi)]; C_SPLAT(); } } while (0)
; DEVI void attn_unit8(const Params& p, char* smem, int unit, int l, int& cvs  , CvRun& crun) {
;     ...
;     for (int T = 0; T + 1 < NTILE; ++T) {
;         const char* Kb = K_lds + s0 * 24576; const int vb = vb0 + s0 * 16384;
;         CvRegs cvr; cv_issue(p, l, cvs, lane, cvr, crun); cvs += (int)gridDim.x * 8;
;         qkt(pB0, pB1, Kb + 12288, qr, r32, hi, cinit);
;         finishSM(pA0, pA1, alA, l_reg, pa0, pa1, pa2, pa3);
;         pv_both(o[0], o[1], vb, pa0, pa1, pa2, pa3);
;         { const bool rr_ = partialSM<false>(pB0, pB1, m_reg, alB); B_RESC(alB, rr_); }
;         cv_finish(smem + 124928 + wid * 2304, lane, cvr);
;         if (cvr.live) asm volatile("s_waitcnt vmcnt(2)" ::: "memory"); else VM0();
;         __syncthreads();
;         if (T + 2 < NTILE) B_DMA(T + 2, s2);
;         qkt(pA0, pA1, K_lds + s1 * 24576, qr, r32, hi, cinit);
;         finishSM(pB0, pB1, alB, l_reg, pa0, pa1, pa2, pa3);
;         pv_both(o[0], o[1], vb + 8192, pa0, pa1, pa2, pa3);
;         { const bool rr_ = partialSM<false>(pA0, pA1, m_reg, alA); B_RESC(alA, rr_); }
;         { const int t = s0; s0 = s1; s1 = s2; s2 = t; }
;     }
.LBB0_716:
	s_add_i32 s54, s54, s86
	s_add_u32 s44, s44, 0x4000
	s_addc_u32 s45, s45, 0
	v_add_f32_e32 v82, v124, v125
	s_add_u32 s12, s12, 0x6000
	v_fmac_f32_e32 v82, v188, v207
	v_add_f32_e32 v188, v126, v127
	s_addc_u32 s13, s13, 0
	v_fmac_f32_e32 v188, v82, v208
	s_cmp_eq_u32 s12, s67

; DEVI CvSlice cv_slice(const Params& p, int l, int s, int lane) {
;     CvSlice c;
;     if (s < NS_W13) {
;         const int e = s >> 9, r = s & 511, hb = r & 7, mat = (r >> 3) & 1, ks = r >> 4;
;         const float* W = mat ? (e < NE ? p.w3 + ((size_t)l * NE + e) * 1024 * 256 : p.ws3 + (size_t)l * 1024 * 256)
;                              : (e < NE ? p.w1 + ((size_t)l * NE + e) * 1024 * 256 : p.ws1 + (size_t)l * 1024 * 256);
;         const int hc0 = hb * 32;
;         c.src = W + hc0 + (lane & 7) * 4; c.ld = 256; c.dst = p.w13t + (size_t)e * 512 * 1024; c.K = 1024;
;         c.r0 = (hc0 >> 7) * 256 + ((hc0 >> 5) & 3) * 32 + mat * 16; c.k0 = ks * 32; c.perm = 0;
;     } else {
;         s -= NS_W13;
;         const int e = s >> 8, r = s & 255, nb = r & 31, ks = r >> 5;
;         const float* W2 = e < NE ? p.w2 + ((size_t)l * NE + e) * 256 * 1024 : p.ws2 + (size_t)l * 256 * 1024;
;         c.src = W2 + nb * 32 + (lane & 7) * 4; c.ld = 1024; c.dst = p.w2t + (size_t)e * 1024 * 256; c.K = 256; c.r0 = (nb >> 3) * 256 + ((nb & 7) >> 1) * 32 + (nb & 1) * 8; c.k0 = ks * 32; c.perm = 1;
;     }
;     return c;
; }
; DEVI void cv_next(const Params& p, int l, int s, int lane, int stride, CvRun& run) {
;     ...
;     run.c = cv_slice(p, l, s, lane); run.left = 0;
;     if ((stride & 511) == 0) {
;         if (s < NS_W13) { const int e = s >> 9, es = stride >> 9; if (e < NE) { run.left = (NE - 1 - e) / es; run.sstep = (long)es * 1024 * 256; run.dstep = (long)es * 512 * 1024; } }
;         else { const int e = (s - NS_W13) >> 8, es = stride >> 8; if (e < NE) { run.left = (NE - 1 - e) / es; run.sstep = (long)es * 256 * 1024; run.dstep = (long)es * 1024 * 256; } } }
; }
; DEVI void cv_issue(const Params& p, int l, int s, int lane, CvRegs& R, CvRun& run) {
;     R.live = s < NS_SLICES ? 1 : 0;
;     if (R.live) { cv_next(p, l, s, lane, (int)gridDim.x * 8, run); R.c = run.c; const int kq = lane >> 3;
	s_cbranch_scc1 .LBB0_718
	s_mov_b32 s6, s89
	s_mov_b32 s89, s61
	v_mov_b32_e32 v207, v202
	s_branch .LBB0_666
.LBB0_718:
	s_mov_b64 s[44:45], 0x4000
	v_lshlrev_b32_e32 v250, 2, v114
	v_mov_b32_e32 v251, 0
	v_lshl_add_u64 v[170:171], s[68:69], 0, v[250:251]
	s_cmp_lt_i32 s54, 0x30300
	s_cselect_b64 s[12:13], -1, 0
	s_cmp_gt_i32 s54, 0x302ff
	s_cbranch_scc1 .LBB0_748
	s_cmp_gt_i32 s56, 0
	s_mov_b64 s[14:15], -1
	s_cbranch_scc1 .LBB0_745
	s_cmp_gt_i32 s54, 0x201ff
	s_cselect_b64 s[14:15], -1, 0
	s_cmp_lt_i32 s54, 0x20200
	s_mov_b64 s[6:7], -1
	s_cbranch_scc1 .LBB0_722
	s_add_i32 s2, s54, 0xfffdfe00
	s_lshr_b32 s8, s2, 8
	s_and_b32 s10, s54, 0xe0
	s_cmp_lt_u32 s2, 0x10000
	s_cselect_b64 s[6:7], -1, 0
	s_lshl_b32 s2, s2, 10
	s_and_b32 s2, s2, 0x3fc0000
	s_and_b64 s[6:7], s[6:7], exec
	s_cselect_b32 s6, 0xc0, s78
	s_cselect_b32 s2, s2, 0
	s_add_u32 s6, s24, s6
	s_addc_u32 s7, s25, 0
	s_load_dwordx2 s[6:7], s[6:7], 0x0
	s_lshl_b32 s2, s2, 2
	s_load_dwordx2 s[18:19], s[24:25], 0x158
	s_waitcnt lgkmcnt(0)
	s_add_u32 s2, s6, s2
	s_addc_u32 s6, s7, 0
	s_lshl_b32 s7, s54, 7
	s_lshl_b32 s11, s54, 5
	s_and_b32 s7, s7, 0xf80
	s_add_u32 s16, s2, s7
	s_addc_u32 s17, s6, 0
	s_lshl_b64 s[6:7], s[8:9], 19
	s_add_u32 s18, s18, s6
	s_addc_u32 s19, s19, s7
	s_lshl_b32 s6, s54, 4
	s_and_b32 s2, s11, 0x300
	s_and_b32 s6, s6, 0x60
	s_or_b32 s2, s2, s6
	s_lshl_b32 s6, s54, 3
	s_and_b32 s6, s6, 8
	s_or_b32 s8, s2, s6
	s_mov_b64 s[6:7], 0

; DEVI int tidx() { int t = threadIdx.x; asm volatile("" : "+v"(t)); __builtin_assume(t >= 0 && t < 512); return t; }
; DEVI unsigned cvt_pk_bf16(float lo, float hi) { unsigned r; asm volatile("v_cvt_pk_bf16_f32 %0, %1, %2" : "=v"(r) : "v"(lo), "v"(hi)); return r; }
; DEVI float bf2f(bf16_t h) { return __uint_as_float(((unsigned)h) << 16); }
; DEVI void attn_unit8(const Params& p, char* smem, int unit, int l, int& cvs  , CvRun& crun) {
;     const int tid = tidx(), wid = __builtin_amdgcn_readfirstlane(tid >> 6), lane = tid & 63, r32 = lane & 31, hi = lane >> 5;
;     const int x8 = unit & 7, v8 = unit >> 3, bh = x8 + 8 * (v8 >> 4), qt = v8 & 15, b = bh >> 3, hh = bh & 7;
;     char* K_lds = smem; char* V_lds = smem + 73728;
;     float* wsx = (float*)(smem + 122880) + wid * 64; float* li_l = wsx; float* al_l = wsx + 32;
;     const bf16_t* Kg = p.kfull + (size_t)bh * S_ * 96; const bf16_t* Vg = p.vfull + (size_t)bh * S_ * 64;
;     const size_t qtok = (size_t)b * S_ + qt * 256 + wid * 32 + r32;
;     bf16x8 qr[6];
;     { const bf16_t* qp = p.qbuf + qtok * 768 + hh * 96 + hi * 8;
; #pragma unroll
;       for (int d0 = 0; d0 < 6; ++d0) qr[d0] = *(const bf16x8*)(qp + d0 * 16);
;       const f32x4 c0 = *(const f32x4*)(p.cs + qtok * 16 + hi * 8), c1 = *(const f32x4*)(p.cs + qtok * 16 + hi * 8 + 4);
;       const f32x4 s0 = *(const f32x4*)(p.sn + qtok * 16 + hi * 8), s1 = *(const f32x4*)(p.sn + qtok * 16 + hi * 8 + 4);
;       float o1[8], o2[8];
; #pragma unroll
;       for (int j = 0; j < 8; ++j) { const float x1 = bf2f((bf16_t)qr[4][j]), x2 = bf2f((bf16_t)qr[5][j]); const float cc = j < 4 ? c0[j] : c1[j - 4], ss = j < 4 ? s0[j] : s1[j - 4];
;           o1[j] = x1 * cc - x2 * ss; o2[j] = x2 * cc + x1 * ss; }
;       u32x4 w1, w2;
; #pragma unroll
;       for (int j = 0; j < 4; ++j) { w1[j] = cvt_pk_bf16(o1[2 * j], o1[2 * j + 1]); w2[j] = cvt_pk_bf16(o2[2 * j], o2[2 * j + 1]); }
;       qr[4] = *(bf16x8*)&w1; qr[5] = *(bf16x8*)&w2; }
.LBB0_2229:
	v_mov_b32_e32 v86, v0
	s_ashr_i32 s5, s87, 4
	v_readfirstlane_b32 s4, v86
	s_lshr_b32 s53, s4, 6
	s_and_b32 s52, s5, -8
	s_and_b32 s8, s4, 0x3fffffc0
	s_load_dwordx4 s[4:7], s[24:25], 0x1a0
	s_load_dwordx4 s[12:15], s[24:25], 0x110
	s_and_b32 s92, s87, 7
	s_ashr_i32 s16, s87, 7
	s_lshl_b32 s8, s8, 2
	s_or_b32 s10, s52, s92
	s_add_i32 s93, s8, 0
	s_ashr_i32 s17, s16, 31
	s_lshl_b32 s8, s87, 5
	s_ashr_i32 s11, s10, 31
	s_lshl_b64 s[16:17], s[16:17], 12
	s_and_b32 s8, s8, 0xf00
	s_and_b32 s2, s62, 7
	s_add_i32 s93, s93, 0x1e000
	s_waitcnt lgkmcnt(0)
	v_mov_b32_e32 v2, s4
	v_mov_b32_e32 v3, s5
	s_lshl_b64 s[4:5], s[10:11], 19
	s_or_b32 s8, s16, s8
	s_lshl_b32 s11, s53, 5
	v_and_b32_e32 v176, 31, v86
	s_add_u32 s48, s8, s11
	v_or_b32_e32 v10, s48, v176
	s_addc_u32 s49, s17, 0
	v_mad_u64_u32 v[2:3], s[16:17], v10, s74, v[2:3]
	v_bfe_u32 v187, v86, 5, 1
	v_mad_i32_i24 v3, s49, v181, v3
	s_mul_i32 s8, s92, 0xc0
	v_mov_b32_e32 v11, s49
	v_lshl_add_u64 v[2:3], v[2:3], 0, s[8:9]
	v_lshlrev_b32_e32 v178, 4, v187
	v_mov_b32_e32 v179, v175
	v_lshl_add_u64 v[26:27], v[2:3], 0, v[178:179]
	v_lshlrev_b64 v[10:11], 6, v[10:11]
	global_load_dwordx4 v[2:5], v[26:27], off offset:128
	global_load_dwordx4 v[6:9], v[26:27], off offset:160
	v_lshl_add_u64 v[12:13], s[12:13], 0, v[10:11]
	v_and_b32_e32 v174, 32, v86
	v_lshl_add_u64 v[10:11], s[14:15], 0, v[10:11]
	v_lshl_add_u64 v[22:23], v[12:13], 0, v[174:175]
	v_lshl_add_u64 v[18:19], v[10:11], 0, v[174:175]
	global_load_dwordx4 v[10:13], v[18:19], off
	global_load_dwordx4 v[14:17], v[22:23], off
	s_nop 0
	global_load_dwordx4 v[18:21], v[18:19], off offset:16
	s_nop 0
	global_load_dwordx4 v[22:25], v[22:23], off offset:16
	s_load_dwordx2 s[50:51], s[24:25], 0x1b0
	global_load_dwordx4 v[150:153], v[26:27], off
	global_load_dwordx4 v[138:141], v[26:27], off offset:32
	global_load_dwordx4 v[134:137], v[26:27], off offset:64
	global_load_dwordx4 v[130:133], v[26:27], off offset:96
	s_mul_hi_i32 s8, s10, 0xc0000
	s_mul_i32 s10, s10, 0xc0000
	s_add_u32 s10, s6, s10
	s_addc_u32 s11, s7, s8
	s_lshl_b32 s61, s53, 10
	s_add_i32 s96, s61, 0
	s_waitcnt lgkmcnt(0)
	s_add_u32 s4, s50, s4
	s_mov_b32 m0, s96
	v_lshlrev_b32_e32 v88, 6, v187
	s_addc_u32 s5, s51, s5
	s_add_i32 s97, s76, s61
	v_lshlrev_b32_e32 v90, 2, v86
	v_and_b32_e32 v91, 63, v86
	v_lshlrev_b32_e32 v93, 4, v91
	v_lshlrev_b32_e32 v92, 3, v91
	v_lshlrev_b32_e32 v94, 1, v91
	s_mov_b32 s8, s9
	s_mov_b32 s12, s9
	s_mov_b32 s13, s9
	s_mov_b32 s14, s9
	s_mov_b32 s15, s9
	s_mov_b32 s16, s9
	s_mov_b32 s17, s9
	s_mov_b32 s18, s9
	s_mov_b32 s19, s9
	s_mov_b32 s20, s9
	s_mov_b32 s21, s9
	s_mov_b32 s22, s9
	s_mov_b32 s23, s9
	s_mulk_i32 s53, 0x900
	v_mov_b32_e32 v83, v175
	v_mov_b32_e32 v85, v175
	v_and_b32_e32 v114, 28, v90
	v_lshl_add_u32 v188, v176, 2, s93
	v_mul_u32_u24_e32 v202, 0x44, v114
	v_bfe_u32 v196, v91, 1, 2
	v_mov_b32_e32 v208, 1.0
	s_mov_b32 s71, s9
	v_mov_b32_e32 v189, v175
	s_waitcnt vmcnt(9)
	v_lshlrev_b32_e32 v27, 16, v2
	s_waitcnt vmcnt(8)
	v_lshlrev_b32_e32 v26, 16, v6
	v_and_b32_e32 v33, 0xffff0000, v2
	v_lshlrev_b32_e32 v35, 16, v3
	s_waitcnt vmcnt(7)
	v_mov_b32_e32 v28, v10
	s_waitcnt vmcnt(6)
	v_mov_b32_e32 v29, v14
	v_mov_b32_e32 v36, v12
	v_mov_b32_e32 v37, v16
	v_mov_b32_e32 v38, v16
	v_mov_b32_e32 v39, v12
	v_and_b32_e32 v3, 0xffff0000, v3
	v_and_b32_e32 v2, 0xffff0000, v7
	v_mov_b32_e32 v16, v13
	v_mov_b32_e32 v12, v17
	v_and_b32_e32 v32, 0xffff0000, v6
	v_lshlrev_b32_e32 v34, 16, v7
	v_pk_mul_f32 v[6:7], v[28:29], v[26:27]
	v_pk_mul_f32 v[16:17], v[16:17], v[2:3]
	v_pk_mul_f32 v[2:3], v[12:13], v[2:3]
	v_mov_b32_e32 v30, v14
	v_mov_b32_e32 v31, v10
	v_sub_f32_e32 v12, v7, v6
	v_sub_f32_e32 v16, v17, v16
	v_add_f32_e32 v17, v2, v3
	v_lshlrev_b32_e32 v3, 16, v4
	v_lshlrev_b32_e32 v2, 16, v8
	s_waitcnt vmcnt(5)
	v_mov_b32_e32 v6, v18
	s_waitcnt vmcnt(4)
	v_mov_b32_e32 v7, v22
	v_pk_mul_f32 v[26:27], v[30:31], v[26:27]
	v_pk_mul_f32 v[6:7], v[6:7], v[2:3]
	v_add_f32_e32 v13, v26, v27
	v_sub_f32_e32 v26, v7, v6
	v_mov_b32_e32 v6, v22
	v_mov_b32_e32 v7, v18
	v_pk_mul_f32 v[2:3], v[6:7], v[2:3]
	v_mov_b32_e32 v22, v19
	v_add_f32_e32 v27, v2, v3
	v_and_b32_e32 v3, 0xffff0000, v4
	v_and_b32_e32 v2, 0xffff0000, v8
	v_mov_b32_e32 v18, v23
	v_pk_mul_f32 v[6:7], v[22:23], v[2:3]
	v_pk_mul_f32 v[2:3], v[18:19], v[2:3]
	v_sub_f32_e32 v8, v7, v6
	v_add_f32_e32 v18, v2, v3
	v_lshlrev_b32_e32 v3, 16, v5
	v_lshlrev_b32_e32 v2, 16, v9
	v_mov_b32_e32 v6, v20
	v_mov_b32_e32 v7, v24
	v_pk_mul_f32 v[6:7], v[6:7], v[2:3]
	v_mov_b32_e32 v14, v11
	v_sub_f32_e32 v19, v7, v6
	v_mov_b32_e32 v6, v24
	v_mov_b32_e32 v7, v20
	v_pk_mul_f32 v[2:3], v[6:7], v[2:3]
	v_mov_b32_e32 v24, v21
	v_add_f32_e32 v6, v2, v3
	v_and_b32_e32 v3, 0xffff0000, v5
	v_and_b32_e32 v2, 0xffff0000, v9
	v_mov_b32_e32 v20, v25
	v_mov_b32_e32 v10, v15
	v_pk_mul_f32 v[4:5], v[24:25], v[2:3]
	v_pk_mul_f32 v[2:3], v[20:21], v[2:3]
	v_pk_mul_f32 v[14:15], v[14:15], v[32:33]
	v_pk_mul_f32 v[10:11], v[10:11], v[32:33]
	v_pk_mul_f32 v[28:29], v[36:37], v[34:35]
	v_pk_mul_f32 v[30:31], v[38:39], v[34:35]
	v_add_f32_e32 v2, v2, v3
	v_sub_f32_e32 v14, v15, v14
	v_add_f32_e32 v10, v10, v11
	v_sub_f32_e32 v11, v29, v28
	v_add_f32_e32 v15, v30, v31
	v_sub_f32_e32 v4, v5, v4
	v_cvt_pk_bf16_f32 v146, v12, v14
	v_cvt_pk_bf16_f32 v142, v13, v10
	v_cvt_pk_bf16_f32 v147, v11, v16
	v_cvt_pk_bf16_f32 v143, v15, v17
	v_cvt_pk_bf16_f32 v148, v26, v8
	v_cvt_pk_bf16_f32 v144, v27, v18
	v_cvt_pk_bf16_f32 v149, v19, v4
	v_cvt_pk_bf16_f32 v145, v6, v2
	v_mul_u32_u24_e32 v2, 0xaaab, v86
	v_lshrrev_b32_e32 v3, 19, v2
	v_mul_lo_u16_e32 v4, 12, v3
	v_sub_u16_e32 v4, v86, v4
	v_lshrrev_b32_e32 v2, 21, v2
; #define LAS __attribute__((address_space(3)))
; DEVI int v_rd_base(int lane) { return ((lane & 3) << 3) | (((lane >> 2) & 3) << 6) | (((lane >> 4) & 1) << 5) | (((lane >> 5) & 1) << 8); }
; #define VM0() asm volatile("s_waitcnt vmcnt(0)" ::: "memory")
; DEVI void attn_unit8(const Params& p, char* smem, int unit, int l, int& cvs  , CvRun& crun) {
;     ...
;     int ksrc[3];
; #pragma unroll
;     for (int i = 0; i < 3; ++i) { const int pc = tid + 512 * i, row = pc / 12, ch = (pc % 12) ^ ((row >> 2) & 3); ksrc[i] = row * 192 + ch * 16; }
;     const int vsrc = wid * 1024 + ((lane >> 2) & 7) * 128 + (lane >> 5) * 64 + (lane & 3) * 16;
;     LAS char* const Kl = (LAS char*)K_lds + wid * 1024; LAS char* const Vl = (LAS char*)V_lds + wid * 1024;
;     ...
;     const int vb0 = (int)(uintptr_t)(LAS char*)V_lds + v_rd_base(lane);
;     float m_reg = 0.f, l_reg = 0.f; f32x16 o[2];
; #pragma unroll
;     for (int d = 0; d < 2; ++d)
; #pragma unroll
;         for (int r = 0; r < 16; ++r) o[d][r] = 0.f;
;     f32x16 pA0, pA1, pB0, pB1; float alA, alB; bf16x8 pa0, pa1, pa2, pa3;
;     constexpr int NTILE = S_ / 128;
;     B_DMA(0, 0); B_DMA(1, 1); VM0(); __syncthreads();
	v_bitop3_b32 v2, v2, v4, 3 bitop3:0x6c
	v_mul_u32_u24_e32 v3, 0xc0, v3
	v_lshl_add_u32 v174, v2, 4, v3
	v_or_b32_e32 v2, 0x200, v86
	v_mul_u32_u24_sdwa v3, v2, s75 dst_sel:DWORD dst_unused:UNUSED_PAD src0_sel:WORD_0 src1_sel:DWORD
	v_lshrrev_b32_e32 v4, 19, v3
	v_mul_lo_u16_e32 v5, 12, v4
	v_sub_u16_e32 v2, v2, v5
	v_lshrrev_b32_e32 v3, 21, v3
	v_bitop3_b32 v2, v3, v2, 3 bitop3:0x6c
	v_mul_u32_u24_e32 v3, 0xc0, v4
	v_lshl_add_u32 v82, v2, 4, v3
	v_or_b32_e32 v2, 0x400, v86
	v_mul_u32_u24_sdwa v3, v2, s75 dst_sel:DWORD dst_unused:UNUSED_PAD src0_sel:WORD_0 src1_sel:DWORD
	v_lshrrev_b32_e32 v4, 19, v3
	v_mul_lo_u16_e32 v5, 12, v4
	v_sub_u16_e32 v2, v2, v5
	v_lshrrev_b32_e32 v3, 21, v3
	v_bitop3_b32 v2, v3, v2, 3 bitop3:0x6c
	v_mul_u32_u24_e32 v3, 0xc0, v4
	v_lshl_add_u32 v84, v2, 4, v3
	v_lshlrev_b32_e32 v2, 5, v86
	v_and_b32_e32 v87, 0x380, v2
	v_lshlrev_b32_e32 v3, 4, v86
	global_load_lds_dwordx4 v174, s[10:11]
	s_add_i32 m0, s96, 0x2000
	v_or_b32_e32 v2, v88, v87
	v_and_b32_e32 v89, 48, v3
	global_load_lds_dwordx4 v82, s[10:11]
	s_add_i32 m0, s96, 0x4000
	v_or3_b32 v2, v2, v89, s61
	global_load_lds_dwordx4 v84, s[10:11]
	v_mov_b32_e32 v3, v175
	s_mov_b32 m0, s97
	v_lshl_add_u64 v[4:5], s[4:5], 0, v[2:3]
	global_load_lds_dwordx4 v2, s[4:5]
	s_add_i32 m0, s97, 0x2000
	v_lshl_add_u64 v[2:3], v[4:5], 0, s[40:41]
	s_add_u32 s4, s10, 0x6000
	global_load_lds_dwordx4 v[2:3], off
	s_addc_u32 s5, s11, 0
	s_add_i32 m0, s96, 0x6000
	v_lshl_add_u64 v[2:3], v[4:5], 0, s[44:45]
	global_load_lds_dwordx4 v174, s[4:5]
	s_add_i32 m0, s96, 0x8000
	v_mul_u32_u24_e32 v10, 0xc0, v176
	global_load_lds_dwordx4 v82, s[4:5]
	s_add_i32 m0, s96, 0xa000
	v_and_b32_e32 v11, 48, v90
	global_load_lds_dwordx4 v84, s[4:5]
	s_add_i32 m0, s97, 0x4000
	v_bitop3_b32 v129, v178, v10, v11 bitop3:0xde
	global_load_lds_dwordx4 v[2:3], off
	v_lshl_add_u64 v[2:3], v[4:5], 0, s[42:43]
	s_add_i32 m0, s97, 0x6000
	v_add_u32_e32 v190, 0, v129
	global_load_lds_dwordx4 v[2:3], off
	s_waitcnt vmcnt(0)
	s_waitcnt vmcnt(0) lgkmcnt(0)
	s_barrier
; #define VM0() asm volatile("s_waitcnt vmcnt(0)" ::: "memory")
; #define C_SPLAT() do { _Pragma("unroll") for (int _r = 0; _r < 16; ++_r) cinit[_r] = -m_reg; asm volatile("" : "+v"(cinit)); } while (0)
; template <bool FIRST> DEVI bool partialSM(f32x16& p0, f32x16& p1, float& m_reg, float& alpha) {
;     float pmax = p0[0];
; #pragma unroll
;     for (int r = 1; r < 16; ++r) pmax = fmaxf(pmax, p0[r]);
; #pragma unroll
;     for (int r = 0; r < 16; ++r) pmax = fmaxf(pmax, p1[r]);
;     { auto rr = __builtin_amdgcn_permlane32_swap(__float_as_uint(pmax), __float_as_uint(pmax), false, false);
;       pmax = fmaxf(__uint_as_float(rr[0]), __uint_as_float(rr[1])); }
;     if (FIRST) { m_reg = pmax; alpha = 1.f;
; #pragma unroll
;         for (int r = 0; r < 16; ++r) { p0[r] = __builtin_amdgcn_exp2f(p0[r] - pmax); p1[r] = p1[r] - pmax; }
;         return false;
; DEVI void attn_unit8(const Params& p, char* smem, int unit, int l, int& cvs  , CvRun& crun) {
;     ...
;     float m_reg = 0.f, l_reg = 0.f; f32x16 o[2];
; #pragma unroll
;     for (int d = 0; d < 2; ++d)
; #pragma unroll
;         for (int r = 0; r < 16; ++r) o[d][r] = 0.f;
;     f32x16 pA0, pA1, pB0, pB1; float alA, alB; bf16x8 pa0, pa1, pa2, pa3;
;     constexpr int NTILE = S_ / 128;
;     B_DMA(0, 0); B_DMA(1, 1); VM0(); __syncthreads();
;     f32x16 cinit;
;     ...
;     { f32x16 z; _Pragma("unroll") for (int r = 0; r < 16; ++r) z[r] = 0.f;
;       qkt(pA0, pA1, K_lds, qr, r32, hi, z); } partialSM<true>(pA0, pA1, m_reg, alA); C_SPLAT();
;     int s0 = 0, s1 = 1, s2 = 2;
	ds_read_b128 v[2:5], v190
	ds_read_b128 v[6:9], v190 offset:6144
	s_waitcnt lgkmcnt(1)
	v_mfma_f32_32x32x16_bf16 v[34:49], v[2:5], v[150:153], 0
	v_or_b32_e32 v2, 32, v178
	v_bitop3_b32 v184, v2, v10, v11 bitop3:0xde
	v_add_u32_e32 v191, 0, v184
	s_mov_b32 s10, s9
	s_mov_b32 s11, s9
	s_lshl_b32 s84, s54, 5
	s_lshl_b32 s85, s54, 4
	s_waitcnt lgkmcnt(0)
	v_mfma_f32_32x32x16_bf16 v[18:33], v[6:9], v[150:153], 0
	ds_read_b128 v[2:5], v191
	ds_read_b128 v[6:9], v191 offset:6144
	s_lshl_b32 s88, s54, 3
	s_lshl_b32 s70, s54, 1
	v_cmp_gt_u32_e64 s[4:5], 32, v91
	s_waitcnt lgkmcnt(1)
	v_mfma_f32_32x32x16_bf16 v[34:49], v[2:5], v[138:141], v[34:49]
	v_or_b32_e32 v2, 64, v178
	v_xad_u32 v185, v2, v11, v10
	v_add_u32_e32 v192, 0, v185
	s_waitcnt lgkmcnt(0)
	v_mfma_f32_32x32x16_bf16 v[18:33], v[6:9], v[138:141], v[18:33]
	ds_read_b128 v[2:5], v192
	ds_read_b128 v[6:9], v192 offset:6144
	s_waitcnt lgkmcnt(1)
	v_mfma_f32_32x32x16_bf16 v[34:49], v[2:5], v[134:137], v[34:49]
	v_or_b32_e32 v2, 0x60, v178
	v_xad_u32 v205, v2, v11, v10
	v_add_u32_e32 v193, 0, v205
	ds_read_b128 v[2:5], v193
	s_waitcnt lgkmcnt(1)
	v_mfma_f32_32x32x16_bf16 v[18:33], v[6:9], v[134:137], v[18:33]
	ds_read_b128 v[6:9], v193 offset:6144
	s_waitcnt lgkmcnt(1)
	v_mfma_f32_32x32x16_bf16 v[34:49], v[2:5], v[130:133], v[34:49]
	v_and_b32_e32 v2, 0xc0, v93
	v_and_or_b32 v12, v92, 24, v2
	v_or_b32_e32 v2, 0x80, v178
	v_xad_u32 v206, v2, v11, v10
	v_add_u32_e32 v194, 0, v206
	ds_read_b128 v[2:5], v194
	s_waitcnt lgkmcnt(1)
	v_mfma_f32_32x32x16_bf16 v[18:33], v[6:9], v[130:133], v[18:33]
	v_and_b32_e32 v6, 32, v94
	v_and_b32_e32 v7, 0x100, v92
	v_or3_b32 v179, v12, v6, v7
	ds_read_b128 v[6:9], v194 offset:6144
	v_add_u32_e32 v115, s76, v179
	s_waitcnt lgkmcnt(1)
	v_mfma_f32_32x32x16_bf16 v[34:49], v[2:5], v[146:149], v[34:49]
	v_or_b32_e32 v2, 0xa0, v178
	v_xad_u32 v207, v2, v11, v10
	v_add_u32_e32 v195, 0, v207
	ds_read_b128 v[2:5], v195
	ds_read_b128 v[50:53], v195 offset:6144
	s_waitcnt lgkmcnt(2)
	v_mfma_f32_32x32x16_bf16 v[18:33], v[6:9], v[146:149], v[18:33]
	s_waitcnt lgkmcnt(1)
	v_mfma_f32_32x32x16_bf16 v[34:49], v[2:5], v[142:145], v[34:49]
	v_mov_b64_e32 v[2:3], s[8:9]
	v_mov_b64_e32 v[4:5], s[10:11]
	v_mov_b64_e32 v[6:7], s[12:13]
	v_mov_b64_e32 v[8:9], s[14:15]
	v_mov_b64_e32 v[10:11], s[16:17]
	v_mov_b64_e32 v[12:13], s[18:19]
	v_mov_b64_e32 v[14:15], s[20:21]
	s_waitcnt lgkmcnt(0)
	v_mfma_f32_32x32x16_bf16 v[18:33], v[50:53], v[142:145], v[18:33]
	s_nop 2
	v_max_f32_e32 v50, v35, v35
	v_max_f32_e32 v51, v34, v34
	v_max_f32_e32 v50, v51, v50
	v_max3_f32 v50, v50, v36, v37
	v_max3_f32 v50, v50, v38, v39
	v_max3_f32 v50, v50, v40, v41
	v_max3_f32 v50, v50, v42, v43
	v_max3_f32 v50, v50, v44, v45
	v_max3_f32 v50, v50, v46, v47
	v_max3_f32 v50, v50, v48, v49
	v_max3_f32 v50, v50, v18, v19
	v_max3_f32 v50, v50, v20, v21
	v_max3_f32 v50, v50, v22, v23
	v_max3_f32 v50, v50, v24, v25
	v_max3_f32 v50, v50, v26, v27
	v_max3_f32 v50, v50, v28, v29
	v_max3_f32 v50, v50, v30, v31
	v_max3_f32 v50, v50, v32, v33
	v_mov_b32_e32 v51, v50
	s_nop 1
	v_permlane32_swap_b32_e32 v50, v51
	v_max_f32_e32 v51, v51, v51
	v_max_f32_e32 v50, v50, v50
	v_max_f32_e32 v204, v50, v51
	v_sub_f32_e32 v34, v34, v204
	v_exp_f32_e32 v50, v34
	v_sub_f32_e32 v34, v35, v204
	v_exp_f32_e32 v51, v34
	v_sub_f32_e32 v34, v36, v204
	v_exp_f32_e32 v52, v34
	v_sub_f32_e32 v34, v37, v204
	v_exp_f32_e32 v53, v34
	v_sub_f32_e32 v34, v38, v204
	v_exp_f32_e32 v54, v34
	v_sub_f32_e32 v34, v39, v204
	v_exp_f32_e32 v55, v34
	v_sub_f32_e32 v34, v40, v204
	v_exp_f32_e32 v56, v34
	v_sub_f32_e32 v34, v41, v204
	v_exp_f32_e32 v57, v34
	v_sub_f32_e32 v34, v42, v204
	v_mov_b64_e32 v[16:17], s[22:23]
	v_exp_f32_e32 v58, v34
	v_sub_f32_e32 v34, v43, v204
	v_sub_f32_e32 v67, v19, v204
	s_add_i32 s8, s53, 0
	v_bfe_u32 v19, v86, 1, 5
	v_exp_f32_e32 v59, v34
	v_sub_f32_e32 v34, v44, v204
	v_sub_f32_e32 v68, v20, v204
	s_add_i32 s8, s8, 0x1e800
	v_and_b32_e32 v20, 28, v19
	s_or_b32 s10, s52, s2
	v_exp_f32_e32 v60, v34
	v_sub_f32_e32 v34, v45, v204
	v_sub_f32_e32 v69, v21, v204
	v_add_u32_e32 v201, s8, v20
	v_mov_b32_e32 v21, s8
	s_lshl_b32 s8, s54, 10
	s_ashr_i32 s11, s10, 31
	v_exp_f32_e32 v61, v34
	v_sub_f32_e32 v34, v46, v204
	s_add_i32 s89, s8, 0xf7f80000
	s_lshl_b64 s[12:13], s[10:11], 19
	v_exp_f32_e32 v62, v34
	v_sub_f32_e32 v34, v47, v204
	v_sub_f32_e32 v66, v18, v204
	v_lshrrev_b32_e32 v18, 2, v86
	s_add_u32 s12, s50, s12
	v_exp_f32_e32 v63, v34
	v_sub_f32_e32 v34, v48, v204
	v_sub_f32_e32 v70, v22, v204
	v_and_b32_e32 v128, 14, v18
	v_lshrrev_b32_e32 v22, 3, v86
	v_and_b32_e32 v18, 12, v18
	s_addc_u32 s13, s51, s13
	s_mul_i32 s8, s10, 0xc0000
	v_exp_f32_e32 v64, v34
	v_sub_f32_e32 v34, v49, v204
	v_mad_u32_u24 v199, v19, s78, v21
	v_and_b32_e32 v19, 0x80, v92
	v_and_b32_e32 v21, 16, v94
	v_and_b32_e32 v22, 4, v22
	v_and_or_b32 v198, v93, s77, v18
	v_or_b32_e32 v18, s61, v87
	s_mul_hi_i32 s2, s10, 0xc0000
	s_add_u32 s6, s6, s8
	v_exp_f32_e32 v65, v34
	v_or3_b32 v197, v19, v22, v21
	v_or3_b32 v18, v18, v88, v89
	v_mov_b32_e32 v19, v175
	s_addc_u32 s2, s7, s2
	v_and_b32_e32 v20, 1, v86

; #define LAS __attribute__((address_space(3)))
; DEVI int v_rd_base(int lane) { return ((lane & 3) << 3) | (((lane >> 2) & 3) << 6) | (((lane >> 4) & 1) << 5) | (((lane >> 5) & 1) << 8); }
; #define VM0() asm volatile("s_waitcnt vmcnt(0)" ::: "memory")
; #define C_SPLAT() do { _Pragma("unroll") for (int _r = 0; _r < 16; ++_r) cinit[_r] = -m_reg; asm volatile("" : "+v"(cinit)); } while (0)
; DEVI void attn_unit8(const Params& p, char* smem, int unit, int l, int& cvs  , CvRun& crun) {
;     ...
;     const int vsrc = wid * 1024 + ((lane >> 2) & 7) * 128 + (lane >> 5) * 64 + (lane & 3) * 16;
;     LAS char* const Kl = (LAS char*)K_lds + wid * 1024; LAS char* const Vl = (LAS char*)V_lds + wid * 1024;
;     ...
;     const int vb0 = (int)(uintptr_t)(LAS char*)V_lds + v_rd_base(lane);
;     float m_reg = 0.f, l_reg = 0.f; f32x16 o[2];
; #pragma unroll
;     for (int d = 0; d < 2; ++d)
; #pragma unroll
;         for (int r = 0; r < 16; ++r) o[d][r] = 0.f;
;     f32x16 pA0, pA1, pB0, pB1; float alA, alB; bf16x8 pa0, pa1, pa2, pa3;
;     constexpr int NTILE = S_ / 128;
;     B_DMA(0, 0); B_DMA(1, 1); VM0(); __syncthreads();
;     f32x16 cinit;
;     ...
;     { f32x16 z; _Pragma("unroll") for (int r = 0; r < 16; ++r) z[r] = 0.f;
;       qkt(pA0, pA1, K_lds, qr, r32, hi, z); } partialSM<true>(pA0, pA1, m_reg, alA); C_SPLAT();
;     int s0 = 0, s1 = 1, s2 = 2;
	s_add_u32 s6, s6, 0xc000
	v_xor_b32_e32 v34, 0x80000000, v204
	v_sub_f32_e32 v81, v33, v204
	v_sub_f32_e32 v80, v32, v204
	v_sub_f32_e32 v79, v31, v204
	v_sub_f32_e32 v78, v30, v204
	v_sub_f32_e32 v77, v29, v204
	v_sub_f32_e32 v76, v28, v204
	v_sub_f32_e32 v75, v27, v204
	v_sub_f32_e32 v74, v26, v204
	v_sub_f32_e32 v73, v25, v204
	v_sub_f32_e32 v72, v24, v204
	v_sub_f32_e32 v71, v23, v204
	v_lshlrev_b32_e32 v200, 5, v20
	v_lshlrev_b32_e32 v180, 4, v20
	v_mov_b32_e32 v116, v18
	v_add_u32_e32 v117, 0x2000, v18
	s_addc_u32 s7, s2, 0
	s_add_u32 s44, s12, 0x8000
	s_addc_u32 s45, s13, 0
	v_mov_b64_e32 v[32:33], v[16:17]
	v_mov_b32_e32 v35, v34
	v_mov_b32_e32 v36, v34
	v_mov_b32_e32 v37, v34
	v_mov_b32_e32 v38, v34
	v_mov_b32_e32 v39, v34
	v_mov_b32_e32 v40, v34
	v_mov_b32_e32 v41, v34
	v_mov_b32_e32 v42, v34
	v_mov_b32_e32 v43, v34
	v_mov_b32_e32 v44, v34
	v_mov_b32_e32 v45, v34
	v_mov_b32_e32 v46, v34
	v_mov_b32_e32 v47, v34
	v_mov_b32_e32 v48, v34
	v_mov_b32_e32 v49, v34
	v_mov_b32_e32 v118, v174
	v_mov_b32_e32 v120, v82
	v_mov_b32_e32 v122, v84
	s_mov_b64 s[12:13], s[6:7]
	s_add_u32 s67, s6, 0xb4000
	v_mov_b64_e32 v[30:31], v[14:15]
	v_mov_b64_e32 v[28:29], v[12:13]
	v_mov_b64_e32 v[26:27], v[10:11]
	v_mov_b64_e32 v[24:25], v[8:9]
	v_mov_b64_e32 v[22:23], v[6:7]
	v_mov_b64_e32 v[20:21], v[4:5]
	v_mov_b64_e32 v[18:19], v[2:3]
	s_mov_b32 s6, 2
	s_mov_b32 s61, 1

; #define VM0() asm volatile("s_waitcnt vmcnt(0)" ::: "memory")
; #define B_RESC(a, rare) do { if (rare) { if (hi == 0) al_l[r32] = (a); asm volatile("s_waitcnt lgkmcnt(0)" ::: "memory"); __builtin_amdgcn_wave_barrier(); \
;         _Pragma("unroll") for (int _d = 0; _d < 2; ++_d) _Pragma("unroll") for (int _r = 0; _r < 16; ++_r) o[_d][_r] *= al_l[crow(_r, hi)]; C_SPLAT(); } } while (0)
; DEVI void attn_unit8(const Params& p, char* smem, int unit, int l, int& cvs  , CvRun& crun) {
;     ...
;     for (int T = 0; T + 1 < NTILE; ++T) {
;         const char* Kb = K_lds + s0 * 24576; const int vb = vb0 + s0 * 16384;
;         CvRegs cvr; cv_issue(p, l, cvs, lane, cvr, crun); cvs += (int)gridDim.x * 8;
;         qkt(pB0, pB1, Kb + 12288, qr, r32, hi, cinit);
;         finishSM(pA0, pA1, alA, l_reg, pa0, pa1, pa2, pa3);
;         pv_both(o[0], o[1], vb, pa0, pa1, pa2, pa3);
;         { const bool rr_ = partialSM<false>(pB0, pB1, m_reg, alB); B_RESC(alB, rr_); }
;         cv_finish(smem + 124928 + wid * 2304, lane, cvr);
;         if (cvr.live) asm volatile("s_waitcnt vmcnt(2)" ::: "memory"); else VM0();
;         __syncthreads();
;         if (T + 2 < NTILE) B_DMA(T + 2, s2);
.LBB0_2266:
	s_mul_i32 s98, s61, 0x6000
	s_add_i32 s98, s96, s98
	s_lshl_b32 s99, s61, 14
	s_add_i32 s99, s97, s99
	s_mul_i32 s6, s2, 0x6000
	s_add_i32 s6, s6, 0
	v_add_u32_e32 v249, s6, v129

; #define VM0() asm volatile("s_waitcnt vmcnt(0)" ::: "memory")
; DEVI void attn_unit8(const Params& p, char* smem, int unit, int l, int& cvs  , CvRun& crun) {
;     ...
;         if (cvr.live) asm volatile("s_waitcnt vmcnt(2)" ::: "memory"); else VM0();
;         __syncthreads();
;         if (T + 2 < NTILE) B_DMA(T + 2, s2);
;         qkt(pA0, pA1, K_lds + s1 * 24576, qr, r32, hi, cinit);
	s_mov_b32 m0, s98
	s_barrier
	ds_read_b128 v[234:237], v249
	ds_read_b128 v[212:215], v249 offset:6144
	global_load_lds_dwordx4 v118, s[12:13]
	s_waitcnt lgkmcnt(1)
	v_mfma_f32_32x32x16_bf16 v[98:113], v[234:237], v[150:153], v[34:49]
	s_add_i32 m0, s98, 0x2000

; DEVI void attn_unit8(const Params& p, char* smem, int unit, int l, int& cvs  , CvRun& crun) {
;     ...
;         if (T + 2 < NTILE) B_DMA(T + 2, s2);
;         qkt(pA0, pA1, K_lds + s1 * 24576, qr, r32, hi, cinit);
	v_add_u32_e32 v126, s6, v184
	global_load_lds_dwordx4 v120, s[12:13]
	s_waitcnt lgkmcnt(0)
	v_mfma_f32_32x32x16_bf16 v[66:81], v[212:215], v[150:153], v[34:49]
	ds_read_b128 v[212:215], v126
	ds_read_b128 v[216:219], v126 offset:6144
	s_add_i32 m0, s98, 0x4000

; #define PK4(P, BASE, OUT) do { u32x4 w = {cvt_pk_bf16(P[BASE + 0], P[BASE + 1]), cvt_pk_bf16(P[BASE + 2], P[BASE + 3]), cvt_pk_bf16(P[BASE + 4], P[BASE + 5]), cvt_pk_bf16(P[BASE + 6], P[BASE + 7])}; \
;     OUT = *reinterpret_cast<bf16x8*>(&w); } while (0)
; DEVI void finishSM(f32x16& p0, f32x16& p1, float alpha, float& l_reg, bf16x8& pa0, bf16x8& pa1, bf16x8& pa2, bf16x8& pa3) {
; #pragma unroll
;     for (int r = 0; r < 16; ++r) p1[r] = __builtin_amdgcn_exp2f(p1[r]);
;     f32x2 s2 = (f32x2){p0[0], p0[1]} + (f32x2){p1[0], p1[1]};
; #pragma unroll
;     for (int r = 2; r < 16; r += 2) s2 += (f32x2){p0[r], p0[r + 1]} + (f32x2){p1[r], p1[r + 1]};
;     float ps = s2[0] + s2[1];
;     { auto rr = __builtin_amdgcn_permlane32_swap(__float_as_uint(ps), __float_as_uint(ps), false, false);
;       ps = __uint_as_float(rr[0]) + __uint_as_float(rr[1]); }
;     l_reg = l_reg * alpha + ps;
;     ...
;     PK4(p0, 0, pa0); PK4(p0, 8, pa1); PK4(p1, 0, pa2); PK4(p1, 8, pa3);
;     ...
; }
; DEVI void qkt(f32x16& p0, f32x16& p1, const char* Kb, const bf16x8 (&qr)[6], int r32, int hi, const f32x16& cinit) {
; #pragma unroll
;     for (int d0 = 0; d0 < 6; ++d0) { const int cb = (d0 * 16 + hi * 8) * 2;
;         const bf16x8 k0 = *(const bf16x8*)(Kb + KSWZ(r32, cb)), k1 = *(const bf16x8*)(Kb + KSWZ(32 + r32, cb));
;         p0 = __builtin_amdgcn_mfma_f32_32x32x16_bf16(k0, qr[d0], d0 == 0 ? cinit : p0, 0, 0, 0);
;         p1 = __builtin_amdgcn_mfma_f32_32x32x16_bf16(k1, qr[d0], d0 == 0 ? cinit : p1, 0, 0, 0); }
; }
	v_add_u32_e32 v126, s6, v185
	global_load_lds_dwordx4 v122, s[12:13]
	s_waitcnt lgkmcnt(1)
	v_mfma_f32_32x32x16_bf16 v[98:113], v[212:215], v[138:141], v[98:113]
	s_mov_b32 m0, s99
	s_nop 0
	global_load_lds_dwordx4 v116, s[44:45]
	s_add_i32 m0, s99, 0x2000
	v_add_u32_e32 v174, 0x2000, v203
	global_load_lds_dwordx4 v117, s[44:45]
	s_waitcnt lgkmcnt(0)
	v_mfma_f32_32x32x16_bf16 v[66:81], v[216:219], v[138:141], v[66:81]
	ds_read_b128 v[212:215], v126
	ds_read_b128 v[216:219], v126 offset:6144
	v_add_u32_e32 v126, s6, v205
	s_waitcnt lgkmcnt(1)
	v_mfma_f32_32x32x16_bf16 v[98:113], v[212:215], v[134:137], v[98:113]
	ds_read_b128 v[212:215], v126
	ds_read_b128 v[220:223], v126 offset:6144
	v_add_u32_e32 v126, s6, v206
	s_waitcnt lgkmcnt(2)
	v_mfma_f32_32x32x16_bf16 v[66:81], v[216:219], v[134:137], v[66:81]
	ds_read_b128 v[216:219], v126
	ds_read_b128 v[224:227], v126 offset:6144
	v_add_u32_e32 v126, s6, v207
	ds_read_b128 v[228:231], v126
	ds_read_b128 v[232:235], v126 offset:6144
	v_add_f32_e32 v126, v50, v82
	v_add_f32_e32 v127, v51, v83
	v_cvt_pk_bf16_f32 v50, v50, v51
	v_cvt_pk_bf16_f32 v51, v52, v53
	s_waitcnt lgkmcnt(5)
	v_mfma_f32_32x32x16_bf16 v[98:113], v[212:215], v[130:133], v[98:113]
	v_add_f32_e64 v212, v52, v84
	v_add_f32_e64 v213, v53, v85
	v_cvt_pk_bf16_f32 v52, v54, v55
	v_cvt_pk_bf16_f32 v53, v56, v57
	v_add_f32_e64 v126, v212, v126
	v_add_f32_e64 v127, v213, v127
	v_add_f32_e64 v212, v54, v86
	v_add_f32_e64 v213, v55, v87
	v_cvt_pk_bf16_f32 v54, v58, v59
	s_waitcnt lgkmcnt(4)
	v_mfma_f32_32x32x16_bf16 v[66:81], v[220:223], v[130:133], v[66:81]
	v_add_f32_e64 v126, v212, v126
	v_add_f32_e64 v127, v213, v127
	v_add_f32_e64 v212, v56, v88
	v_add_f32_e64 v213, v57, v89
	v_cvt_pk_bf16_f32 v55, v60, v61
	v_cvt_pk_bf16_f32 v56, v62, v63
	v_cvt_pk_bf16_f32 v57, v64, v65
	v_add_f32_e64 v126, v212, v126
	v_add_f32_e64 v127, v213, v127
	v_add_f32_e32 v212, v58, v90
	v_add_f32_e32 v213, v59, v91
	v_cvt_pk_bf16_f32 v58, v82, v83
	v_cvt_pk_bf16_f32 v59, v84, v85
	s_waitcnt lgkmcnt(3)
	v_mfma_f32_32x32x16_bf16 v[98:113], v[216:219], v[146:149], v[98:113]
	v_add_f32_e64 v126, v212, v126
	v_add_f32_e64 v127, v213, v127
	v_add_f32_e64 v212, v60, v92
	v_add_f32_e64 v213, v61, v93
	v_cvt_pk_bf16_f32 v60, v86, v87
	v_cvt_pk_bf16_f32 v61, v88, v89
	v_add_f32_e64 v126, v212, v126
	v_add_f32_e64 v127, v213, v127
	v_add_f32_e32 v212, v62, v94
	v_add_f32_e32 v213, v63, v95
	v_cvt_pk_bf16_f32 v62, v90, v91
	v_cvt_pk_bf16_f32 v63, v92, v93
	s_waitcnt lgkmcnt(2)
	v_mfma_f32_32x32x16_bf16 v[66:81], v[224:227], v[146:149], v[66:81]
	v_add_f32_e64 v126, v212, v126
	v_add_f32_e64 v127, v213, v127
	v_add_f32_e64 v212, v64, v96
	v_add_f32_e64 v213, v65, v97
	v_cvt_pk_bf16_f32 v64, v94, v95
	v_cvt_pk_bf16_f32 v65, v96, v97
	ds_read_b64_tr_b16 v[154:155], v174 offset:0
	ds_read_b64_tr_b16 v[156:157], v174 offset:0x400
	ds_read_b64_tr_b16 v[158:159], v174 offset:0x800
	ds_read_b64_tr_b16 v[160:161], v174 offset:0xc00
	ds_read_b64_tr_b16 v[162:163], v174 offset:0x1000
	ds_read_b64_tr_b16 v[164:165], v174 offset:0x1400
	ds_read_b64_tr_b16 v[166:167], v174 offset:0x1800
	ds_read_b64_tr_b16 v[168:169], v174 offset:0x1c00
	v_add_f32_e64 v126, v212, v126
	v_add_f32_e64 v127, v213, v127
	ds_read_b64_tr_b16 v[212:213], v174 offset:0x200
	ds_read_b64_tr_b16 v[214:215], v174 offset:0x600
	ds_read_b64_tr_b16 v[216:217], v174 offset:0xa00
	s_waitcnt lgkmcnt(12)
	v_mfma_f32_32x32x16_bf16 v[98:113], v[228:231], v[142:145], v[98:113]
	ds_read_b64_tr_b16 v[218:219], v174 offset:0xe00
	ds_read_b64_tr_b16 v[220:221], v174 offset:0x1200
	ds_read_b64_tr_b16 v[222:223], v174 offset:0x1600
	ds_read_b64_tr_b16 v[224:225], v174 offset:0x1a00
	ds_read_b64_tr_b16 v[226:227], v174 offset:0x1e00
	v_add_f32_e32 v126, v126, v127
	s_waitcnt lgkmcnt(15)
	v_mfma_f32_32x32x16_bf16 v[66:81], v[232:235], v[142:145], v[66:81]
	v_mov_b32_e32 v127, v126


; DEVI void pv_both(f32x16& o0, f32x16& o1, int vb, bf16x8 pa0, bf16x8 pa1, bf16x8 pa2, bf16x8 pa3) {
;     const s16x4 a0 = tr_read<v_rd_off(0, 0, 0)>(vb), b0 = tr_read<v_rd_off(0, 0, 1)>(vb), a1 = tr_read<v_rd_off(0, 1, 0)>(vb), b1 = tr_read<v_rd_off(0, 1, 1)>(vb);
;     const s16x4 a2 = tr_read<v_rd_off(0, 2, 0)>(vb), b2 = tr_read<v_rd_off(0, 2, 1)>(vb), a3 = tr_read<v_rd_off(0, 3, 0)>(vb), b3 = tr_read<v_rd_off(0, 3, 1)>(vb);
;     const s16x4 c0 = tr_read<v_rd_off(1, 0, 0)>(vb), d0 = tr_read<v_rd_off(1, 0, 1)>(vb), c1 = tr_read<v_rd_off(1, 1, 0)>(vb), d1 = tr_read<v_rd_off(1, 1, 1)>(vb);
;     const s16x4 c2 = tr_read<v_rd_off(1, 2, 0)>(vb), d2 = tr_read<v_rd_off(1, 2, 1)>(vb), c3 = tr_read<v_rd_off(1, 3, 0)>(vb), d3 = tr_read<v_rd_off(1, 3, 1)>(vb);
;     asm volatile("s_waitcnt lgkmcnt(8)" ::: "memory"); SBAR();
;     ...
;     o0 = __builtin_amdgcn_mfma_f32_32x32x16_bf16(pa0, PK(a0, b0), o0, 0, 0, 0);
;     o0 = __builtin_amdgcn_mfma_f32_32x32x16_bf16(pa1, PK(a1, b1), o0, 0, 0, 0);
;     o0 = __builtin_amdgcn_mfma_f32_32x32x16_bf16(pa2, PK(a2, b2), o0, 0, 0, 0);
;     o0 = __builtin_amdgcn_mfma_f32_32x32x16_bf16(pa3, PK(a3, b3), o0, 0, 0, 0);
;     asm volatile("s_waitcnt lgkmcnt(0)" ::: "memory"); SBAR();
;     o1 = __builtin_amdgcn_mfma_f32_32x32x16_bf16(pa0, PK(c0, d0), o1, 0, 0, 0);
;     o1 = __builtin_amdgcn_mfma_f32_32x32x16_bf16(pa1, PK(c1, d1), o1, 0, 0, 0);
;     o1 = __builtin_amdgcn_mfma_f32_32x32x16_bf16(pa2, PK(c2, d2), o1, 0, 0, 0);
;     o1 = __builtin_amdgcn_mfma_f32_32x32x16_bf16(pa3, PK(c3, d3), o1, 0, 0, 0);
;     ...
; }
; template <bool FIRST> DEVI bool partialSM(f32x16& p0, f32x16& p1, float& m_reg, float& alpha) {
;     float pmax = p0[0];
; #pragma unroll
;     for (int r = 1; r < 16; ++r) pmax = fmaxf(pmax, p0[r]);
; #pragma unroll
;     for (int r = 0; r < 16; ++r) pmax = fmaxf(pmax, p1[r]);
;     { auto rr = __builtin_amdgcn_permlane32_swap(__float_as_uint(pmax), __float_as_uint(pmax), false, false);
;       pmax = fmaxf(__uint_as_float(rr[0]), __uint_as_float(rr[1])); }
;     if (FIRST) { m_reg = pmax; alpha = 1.f;
; #pragma unroll
;         for (int r = 0; r < 16; ++r) { p0[r] = __builtin_amdgcn_exp2f(p0[r] - pmax); p1[r] = p1[r] - pmax; }
;         return false;
;     } else if (__builtin_expect(__all(pmax <= ATT_THR), 1)) { alpha = 1.f;
; #pragma unroll
;         for (int r = 0; r < 16; ++r) p0[r] = __builtin_amdgcn_exp2f(p0[r]);
	s_waitcnt lgkmcnt(14)
	v_mfma_f32_32x32x16_bf16 v[18:33], v[50:53], v[154:157], v[18:33]
	v_permlane32_swap_b32_e32 v126, v127
	s_waitcnt lgkmcnt(6)
	v_mfma_f32_32x32x16_bf16 v[2:17], v[50:53], v[212:215], v[2:17]
	s_nop 1
	v_max_f32_e32 v249, v99, v99
	v_max_f32_e32 v250, v98, v98
	v_max_f32_e32 v249, v250, v249
	v_max3_f32 v249, v249, v100, v101
	v_max3_f32 v249, v249, v102, v103
	v_max3_f32 v251, v249, v104, v105
	v_max3_f32 v251, v251, v106, v107
	v_exp_f32_e32 v50, v98
	v_exp_f32_e32 v51, v99
	v_exp_f32_e32 v52, v100
	v_exp_f32_e32 v53, v101
	v_mfma_f32_32x32x16_bf16 v[18:33], v[54:57], v[158:161], v[18:33]
	s_waitcnt lgkmcnt(4)
	v_mfma_f32_32x32x16_bf16 v[2:17], v[54:57], v[216:219], v[2:17]
	v_max3_f32 v251, v251, v108, v109
	v_max3_f32 v251, v251, v110, v111
	v_max3_f32 v251, v251, v112, v113
	v_max3_f32 v251, v251, v66, v67
	v_max3_f32 v251, v251, v68, v69
	v_max3_f32 v251, v251, v70, v71
	v_max3_f32 v251, v251, v72, v73
	v_exp_f32_e32 v54, v102
	v_exp_f32_e32 v55, v103
	v_exp_f32_e32 v56, v104
	v_exp_f32_e32 v57, v105
	v_mfma_f32_32x32x16_bf16 v[18:33], v[58:61], v[162:165], v[18:33]
	s_waitcnt lgkmcnt(2)
	v_mfma_f32_32x32x16_bf16 v[2:17], v[58:61], v[220:223], v[2:17]
	v_max3_f32 v251, v251, v74, v75
	v_max3_f32 v251, v251, v76, v77
	v_max3_f32 v251, v251, v78, v79
	v_max3_f32 v251, v251, v80, v81
	v_mov_b32_e32 v252, v251


; #define SBAR() __builtin_amdgcn_sched_barrier(0)
; DEVI void pv_both(f32x16& o0, f32x16& o1, int vb, bf16x8 pa0, bf16x8 pa1, bf16x8 pa2, bf16x8 pa3) {
;     ...
;     o0 = __builtin_amdgcn_mfma_f32_32x32x16_bf16(pa0, PK(a0, b0), o0, 0, 0, 0);
;     o0 = __builtin_amdgcn_mfma_f32_32x32x16_bf16(pa1, PK(a1, b1), o0, 0, 0, 0);
;     o0 = __builtin_amdgcn_mfma_f32_32x32x16_bf16(pa2, PK(a2, b2), o0, 0, 0, 0);
;     o0 = __builtin_amdgcn_mfma_f32_32x32x16_bf16(pa3, PK(a3, b3), o0, 0, 0, 0);
;     asm volatile("s_waitcnt lgkmcnt(0)" ::: "memory"); SBAR();
;     o1 = __builtin_amdgcn_mfma_f32_32x32x16_bf16(pa0, PK(c0, d0), o1, 0, 0, 0);
;     o1 = __builtin_amdgcn_mfma_f32_32x32x16_bf16(pa1, PK(c1, d1), o1, 0, 0, 0);
;     o1 = __builtin_amdgcn_mfma_f32_32x32x16_bf16(pa2, PK(c2, d2), o1, 0, 0, 0);
;     o1 = __builtin_amdgcn_mfma_f32_32x32x16_bf16(pa3, PK(c3, d3), o1, 0, 0, 0);
; template <bool FIRST> DEVI bool partialSM(f32x16& p0, f32x16& p1, float& m_reg, float& alpha) {
;     float pmax = p0[0];
; #pragma unroll
;     for (int r = 1; r < 16; ++r) pmax = fmaxf(pmax, p0[r]);
; #pragma unroll
;     for (int r = 0; r < 16; ++r) pmax = fmaxf(pmax, p1[r]);
;     { auto rr = __builtin_amdgcn_permlane32_swap(__float_as_uint(pmax), __float_as_uint(pmax), false, false);
;       pmax = fmaxf(__uint_as_float(rr[0]), __uint_as_float(rr[1])); }
;     if (FIRST) { m_reg = pmax; alpha = 1.f;
; #pragma unroll
;         for (int r = 0; r < 16; ++r) { p0[r] = __builtin_amdgcn_exp2f(p0[r] - pmax); p1[r] = p1[r] - pmax; }
;         return false;
;     } else if (__builtin_expect(__all(pmax <= ATT_THR), 1)) { alpha = 1.f;
; #pragma unroll
;         for (int r = 0; r < 16; ++r) p0[r] = __builtin_amdgcn_exp2f(p0[r]);
	v_exp_f32_e32 v58, v106
	v_exp_f32_e32 v59, v107
	v_permlane32_swap_b32_e32 v251, v252
	v_exp_f32_e32 v60, v108
	v_exp_f32_e32 v61, v109
	v_mfma_f32_32x32x16_bf16 v[18:33], v[62:65], v[166:169], v[18:33]
	s_waitcnt lgkmcnt(0)
	v_mfma_f32_32x32x16_bf16 v[2:17], v[62:65], v[224:227], v[2:17]
	v_exp_f32_e32 v62, v110
	v_exp_f32_e32 v63, v111
	v_exp_f32_e32 v64, v112
	v_exp_f32_e32 v65, v113
	v_max_f32_e32 v252, v252, v252
	v_max_f32_e32 v251, v251, v251
	v_max_f32_e32 v174, v251, v252
	v_cmp_ge_f32_e32 vcc, s80, v174
	s_cmp_lg_u64 vcc, exec
	s_cselect_b64 s[6:7], -1, 0
	s_cbranch_scc1 .LBB0_2275
	v_mov_b32_e32 v203, 1.0
	v_mov_b32_e32 v204, v210
	s_branch .LBB0_2280

; #define VM0() asm volatile("s_waitcnt vmcnt(0)" ::: "memory")
; #define B_RESC(a, rare) do { if (rare) { if (hi == 0) al_l[r32] = (a); asm volatile("s_waitcnt lgkmcnt(0)" ::: "memory"); __builtin_amdgcn_wave_barrier(); \
;         _Pragma("unroll") for (int _d = 0; _d < 2; ++_d) _Pragma("unroll") for (int _r = 0; _r < 16; ++_r) o[_d][_r] *= al_l[crow(_r, hi)]; C_SPLAT(); } } while (0)
; DEVI void attn_unit8(const Params& p, char* smem, int unit, int l, int& cvs  , CvRun& crun) {
;     ...
;     for (int T = 0; T + 1 < NTILE; ++T) {
;         const char* Kb = K_lds + s0 * 24576; const int vb = vb0 + s0 * 16384;
;         CvRegs cvr; cv_issue(p, l, cvs, lane, cvr, crun); cvs += (int)gridDim.x * 8;
;         qkt(pB0, pB1, Kb + 12288, qr, r32, hi, cinit);
;         finishSM(pA0, pA1, alA, l_reg, pa0, pa1, pa2, pa3);
;         pv_both(o[0], o[1], vb, pa0, pa1, pa2, pa3);
;         { const bool rr_ = partialSM<false>(pB0, pB1, m_reg, alB); B_RESC(alB, rr_); }
;         cv_finish(smem + 124928 + wid * 2304, lane, cvr);
;         if (cvr.live) asm volatile("s_waitcnt vmcnt(2)" ::: "memory"); else VM0();
;         __syncthreads();
;         if (T + 2 < NTILE) B_DMA(T + 2, s2);
;         qkt(pA0, pA1, K_lds + s1 * 24576, qr, r32, hi, cinit);
;         finishSM(pB0, pB1, alB, l_reg, pa0, pa1, pa2, pa3);
;         pv_both(o[0], o[1], vb + 8192, pa0, pa1, pa2, pa3);
;         { const bool rr_ = partialSM<false>(pA0, pA1, m_reg, alA); B_RESC(alA, rr_); }
;         { const int t = s0; s0 = s1; s1 = s2; s2 = t; }
;     }
.LBB0_2280:
	s_add_i32 s54, s54, s86
	s_add_u32 s44, s44, 0x4000
	s_addc_u32 s45, s45, 0
	v_add_f32_e32 v82, v124, v125
	s_add_u32 s12, s12, 0x6000
	v_fmac_f32_e32 v82, v189, v208
	v_add_f32_e32 v189, v126, v127
	s_addc_u32 s13, s13, 0
	v_fmac_f32_e32 v189, v82, v209
	s_cmp_eq_u32 s12, s67

; DEVI CvSlice cv_slice(const Params& p, int l, int s, int lane) {
;     CvSlice c;
;     if (s < NS_W13) {
;         const int e = s >> 9, r = s & 511, hb = r & 7, mat = (r >> 3) & 1, ks = r >> 4;
;         const float* W = mat ? (e < NE ? p.w3 + ((size_t)l * NE + e) * 1024 * 256 : p.ws3 + (size_t)l * 1024 * 256)
;                              : (e < NE ? p.w1 + ((size_t)l * NE + e) * 1024 * 256 : p.ws1 + (size_t)l * 1024 * 256);
;         const int hc0 = hb * 32;
;         c.src = W + hc0 + (lane & 7) * 4; c.ld = 256; c.dst = p.w13t + (size_t)e * 512 * 1024; c.K = 1024;
;         c.r0 = (hc0 >> 7) * 256 + ((hc0 >> 5) & 3) * 32 + mat * 16; c.k0 = ks * 32; c.perm = 0;
;     } else {
;         s -= NS_W13;
;         const int e = s >> 8, r = s & 255, nb = r & 31, ks = r >> 5;
;         const float* W2 = e < NE ? p.w2 + ((size_t)l * NE + e) * 256 * 1024 : p.ws2 + (size_t)l * 256 * 1024;
;         c.src = W2 + nb * 32 + (lane & 7) * 4; c.ld = 1024; c.dst = p.w2t + (size_t)e * 1024 * 256; c.K = 256; c.r0 = (nb >> 3) * 256 + ((nb & 7) >> 1) * 32 + (nb & 1) * 8; c.k0 = ks * 32; c.perm = 1;
;     }
;     return c;
; }
; DEVI void cv_next(const Params& p, int l, int s, int lane, int stride, CvRun& run) {
;     ...
;     run.c = cv_slice(p, l, s, lane); run.left = 0;
;     if ((stride & 511) == 0) {
;         if (s < NS_W13) { const int e = s >> 9, es = stride >> 9; if (e < NE) { run.left = (NE - 1 - e) / es; run.sstep = (long)es * 1024 * 256; run.dstep = (long)es * 512 * 1024; } }
;         else { const int e = (s - NS_W13) >> 8, es = stride >> 8; if (e < NE) { run.left = (NE - 1 - e) / es; run.sstep = (long)es * 256 * 1024; run.dstep = (long)es * 1024 * 256; } } }
; }
; DEVI void cv_issue(const Params& p, int l, int s, int lane, CvRegs& R, CvRun& run) {
;     R.live = s < NS_SLICES ? 1 : 0;
;     if (R.live) { cv_next(p, l, s, lane, (int)gridDim.x * 8, run); R.c = run.c; const int kq = lane >> 3;
	s_cbranch_scc1 .LBB0_2282
	s_mov_b32 s6, s71
	s_mov_b32 s71, s2
	v_mov_b32_e32 v208, v203
	s_branch .LBB0_2230
.LBB0_2282:
	s_mov_b64 s[44:45], 0x4000
	v_lshlrev_b32_e32 v250, 2, v114
	v_mov_b32_e32 v251, 0
	v_lshl_add_u64 v[170:171], s[68:69], 0, v[250:251]
	s_cmp_lt_i32 s54, 0x30300
	s_cselect_b64 s[12:13], -1, 0
	s_cmp_gt_i32 s54, 0x302ff
	s_cbranch_scc1 .LBB0_2312
	s_cmp_gt_i32 s56, 0
	s_mov_b64 s[14:15], -1
	s_cbranch_scc1 .LBB0_2309
	s_cmp_gt_i32 s54, 0x201ff
	s_cselect_b64 s[14:15], -1, 0
	s_cmp_lt_i32 s54, 0x20200
	s_mov_b64 s[6:7], -1
	s_cbranch_scc1 .LBB0_2286
	s_add_i32 s2, s54, 0xfffdfe00
	s_lshr_b32 s8, s2, 8
	s_and_b32 s10, s54, 0xe0
	s_cmp_lt_u32 s2, 0x10000
	s_cselect_b64 s[6:7], -1, 0
	s_lshl_b32 s2, s2, 10
	s_and_b32 s2, s2, 0x3fc0000
	s_bitset1_b32 s2, 26
	s_and_b64 s[6:7], s[6:7], exec
	s_cselect_b32 s6, 0xc0, s79
	s_cselect_b32 s2, s2, 0x40000
	s_add_u32 s6, s24, s6
	s_addc_u32 s7, s25, 0
	s_load_dwordx2 s[6:7], s[6:7], 0x0
	s_lshl_b32 s2, s2, 2
	s_load_dwordx2 s[18:19], s[24:25], 0x158
	s_waitcnt lgkmcnt(0)
	s_add_u32 s2, s6, s2
	s_addc_u32 s6, s7, 0
	s_lshl_b32 s7, s54, 7
	s_lshl_b32 s11, s54, 5
	s_and_b32 s7, s7, 0xf80
	s_add_u32 s16, s2, s7
	s_addc_u32 s17, s6, 0
	s_lshl_b64 s[6:7], s[8:9], 19
	s_add_u32 s18, s18, s6
	s_addc_u32 s19, s19, s7
	s_lshl_b32 s6, s54, 4
	s_and_b32 s2, s11, 0x300
	s_and_b32 s6, s6, 0x60
	s_or_b32 s2, s2, s6
	s_lshl_b32 s6, s54, 3
	s_and_b32 s6, s6, 8
	s_or_b32 s8, s2, s6
	s_mov_b64 s[6:7], 0
